# speedup vs baseline: 1.0323x; 1.0323x over previous
.LBB1_7:
.LBB1_8:
	v_max_f32_e32 v50, v67, v67
	v_max_f32_e32 v51, v66, v66
	v_max_f32_e32 v50, v51, v50
	v_max3_f32 v51, v68, v69, v83
	v_max3_f32 v50, v50, v82, v84
	v_max3_f32 v50, v50, v85, v70
	v_max3_f32 v51, v51, v72, v73
	v_max3_f32 v50, v50, v71, v86
	v_max3_f32 v51, v51, v88, v89
	v_max3_f32 v50, v50, v87, v74
	v_max3_f32 v51, v51, v76, v77
	v_max3_f32 v50, v50, v75, v90
	v_max3_f32 v51, v51, v92, v93
	v_max3_f32 v50, v50, v91, v78
	v_max3_f32 v51, v51, v80, v81
	v_max3_f32 v50, v50, v79, v94
	v_max3_f32 v51, v51, v96, v97
	v_max3_f32 v50, v50, v95, v51
	v_mov_b32_e32 v51, v50
	s_nop 1
	v_permlane32_swap_b32_e32 v50, v51
	v_max_f32_e32 v51, v51, v51
	v_max_f32_e32 v50, v50, v50
	v_max_f32_e32 v50, v50, v51
	v_cmp_lt_f32_e32 vcc, s47, v50
	s_cmp_lg_u64 vcc, 0
	v_add_f32_e32 v181, v218, v160
	s_cselect_b64 s[2:3], -1, 0
	s_cbranch_vccnz .LBB1_21
.LBB1_9:
	s_xor_b64 s[30:31], s[20:21], -1
	s_waitcnt lgkmcnt(14)
	v_mfma_f32_32x32x16_f16 v[18:33], v[128:131], v[172:175], v[18:33]
	v_exp_f32_e32 v66, v66
	v_exp_f32_e32 v67, v67
	v_exp_f32_e32 v68, v68
	v_exp_f32_e32 v69, v69
	s_waitcnt lgkmcnt(12)
	v_mfma_f32_32x32x16_f16 v[2:17], v[128:131], v[176:179], v[2:17]
	v_exp_f32_e32 v70, v70
	v_exp_f32_e32 v71, v71
	v_exp_f32_e32 v72, v72
	v_exp_f32_e32 v73, v73
	v_add_u32_e32 v54, s45, v217
	v_add_u32_e32 v55, v54, v207
	ds_read_b128 v[50:53], v55
	ds_read_b128 v[34:37], v55 offset:4096
	s_waitcnt lgkmcnt(12)
	v_mfma_f32_32x32x16_f16 v[18:33], v[106:109], v[122:125], v[18:33]
	v_exp_f32_e32 v74, v74
	v_exp_f32_e32 v75, v75
	v_exp_f32_e32 v76, v76
	v_exp_f32_e32 v77, v77
	v_add_u32_e32 v55, v54, v206
	ds_read_b128 v[122:125], v55
	ds_read_b128 v[172:175], v55 offset:4096
	s_waitcnt lgkmcnt(12)
	v_mfma_f32_32x32x16_f16 v[2:17], v[106:109], v[118:121], v[2:17]
	v_exp_f32_e32 v78, v78
	v_exp_f32_e32 v79, v79
	v_exp_f32_e32 v80, v80
	v_exp_f32_e32 v81, v81
	v_add_u32_e32 v55, v54, v205
	ds_read_b128 v[176:179], v55
	ds_read_b128 v[164:167], v55 offset:4096
	s_waitcnt lgkmcnt(12)
	v_mfma_f32_32x32x16_f16 v[18:33], v[102:105], v[114:117], v[18:33]
	v_exp_f32_e32 v82, v82
	v_exp_f32_e32 v83, v83
	v_exp_f32_e32 v84, v84
	v_exp_f32_e32 v85, v85
	v_add_u32_e32 v54, v54, v204
	ds_read_b128 v[168:171], v54
	ds_read_b128 v[160:163], v54 offset:4096
	s_waitcnt lgkmcnt(12)
	v_mfma_f32_32x32x16_f16 v[2:17], v[102:105], v[110:113], v[2:17]
	v_exp_f32_e32 v86, v86
	v_exp_f32_e32 v87, v87
	v_exp_f32_e32 v88, v88
	v_exp_f32_e32 v89, v89
	s_waitcnt lgkmcnt(10)
	v_mfma_f32_32x32x16_f16 v[18:33], v[98:101], v[156:159], v[18:33]
	v_exp_f32_e32 v90, v90
	v_exp_f32_e32 v91, v91
	v_exp_f32_e32 v92, v92
	v_exp_f32_e32 v93, v93
	s_waitcnt lgkmcnt(8)
	v_mfma_f32_32x32x16_f16 v[2:17], v[98:101], v[152:155], v[2:17]
	v_exp_f32_e32 v94, v94
	v_exp_f32_e32 v95, v95
	v_exp_f32_e32 v96, v96
	v_exp_f32_e32 v97, v97
	s_waitcnt vmcnt(4) lgkmcnt(0)
	s_barrier
	s_andn2_b64 vcc, exec, s[2:3]
	s_cbranch_vccnz .LBB1_11
	ds_read_b128 v[54:57], v213 offset:96
	ds_read_b128 v[58:61], v213 offset:64
	ds_read_b128 v[62:65], v213 offset:32
	ds_read_b128 v[38:41], v213
	s_waitcnt lgkmcnt(3)
	v_pk_mul_f32 v[32:33], v[32:33], v[56:57]
	s_waitcnt lgkmcnt(2)
	v_pk_mul_f32 v[28:29], v[28:29], v[60:61]
	s_waitcnt lgkmcnt(1)
	v_pk_mul_f32 v[24:25], v[24:25], v[64:65]
	s_waitcnt lgkmcnt(0)
	v_pk_mul_f32 v[20:21], v[20:21], v[40:41]
	v_pk_mul_f32 v[30:31], v[30:31], v[54:55]
	v_pk_mul_f32 v[26:27], v[26:27], v[58:59]
	v_pk_mul_f32 v[22:23], v[22:23], v[62:63]
	v_pk_mul_f32 v[18:19], v[18:19], v[38:39]
	v_pk_mul_f32 v[16:17], v[16:17], v[56:57]
	v_pk_mul_f32 v[12:13], v[12:13], v[60:61]
	v_pk_mul_f32 v[8:9], v[8:9], v[64:65]
	v_pk_mul_f32 v[4:5], v[4:5], v[40:41]
	v_pk_mul_f32 v[14:15], v[14:15], v[54:55]
	v_pk_mul_f32 v[10:11], v[10:11], v[58:59]
	v_pk_mul_f32 v[6:7], v[6:7], v[62:63]
	v_pk_mul_f32 v[2:3], v[2:3], v[38:39]
.LBB1_11:
	s_add_i32 s2, s45, 0x4000
	s_cmpk_lg_u32 s45, 0x8000
	s_cselect_b32 s43, s2, 0
	v_add_u32_e32 v156, s48, v215
	ds_read_b64_tr_b16 v[118:119], v156 offset:49152
	ds_read_b64_tr_b16 v[120:121], v156 offset:49664
	v_add_f32_e32 v54, v66, v67
	v_add_f32_e32 v54, v68, v54
	v_add_f32_e32 v54, v69, v54
	v_add_f32_e32 v54, v70, v54
	v_add_f32_e32 v38, v71, v54
	s_waitcnt lgkmcnt(9)
	v_mfma_f32_32x32x16_f16 v[50:65], v[50:53], v[144:147], 0
	v_cvt_pk_f16_f32 v128, v66, v67
	v_cvt_pk_f16_f32 v129, v68, v69
	s_nop 0
	ds_read_b64_tr_b16 v[152:153], v156 offset:53248
	ds_read_b64_tr_b16 v[154:155], v156 offset:53760
	v_add_f32_e32 v66, v72, v38
	s_waitcnt lgkmcnt(10)
	v_mfma_f32_32x32x16_f16 v[34:49], v[34:37], v[144:147], 0
	v_add_f32_e32 v66, v73, v66
	v_add_f32_e32 v66, v74, v66
	v_add_f32_e32 v66, v75, v66
	v_cvt_pk_f16_f32 v130, v70, v71
	v_cvt_pk_f16_f32 v131, v72, v73
	s_nop 0
	ds_read_b64_tr_b16 v[148:149], v156 offset:50176
	ds_read_b64_tr_b16 v[150:151], v156 offset:50688
	s_waitcnt lgkmcnt(11)
	v_mfma_f32_32x32x16_f16 v[50:65], v[122:125], v[140:143], v[50:65]
	v_add_f32_e32 v66, v76, v66
	v_add_f32_e32 v66, v77, v66
	v_add_f32_e32 v66, v78, v66
	v_add_f32_e32 v66, v79, v66
	v_cvt_pk_f16_f32 v106, v74, v75
	v_cvt_pk_f16_f32 v107, v76, v77
	s_nop 0
	ds_read_b64_tr_b16 v[122:123], v156 offset:54272
	ds_read_b64_tr_b16 v[124:125], v156 offset:54784
	s_waitcnt lgkmcnt(12)
	v_mfma_f32_32x32x16_f16 v[34:49], v[172:175], v[140:143], v[34:49]
	v_add_f32_e32 v66, v80, v66
	v_add_f32_e32 v66, v81, v66
	v_add_f32_e32 v66, v82, v66
	v_add_f32_e32 v66, v83, v66
	v_cvt_pk_f16_f32 v108, v78, v79
	v_cvt_pk_f16_f32 v109, v80, v81
	s_nop 0
	ds_read_b64_tr_b16 v[114:115], v156 offset:51200
	ds_read_b64_tr_b16 v[116:117], v156 offset:51712
	s_waitcnt lgkmcnt(13)
	v_mfma_f32_32x32x16_f16 v[50:65], v[176:179], v[136:139], v[50:65]
	v_add_f32_e32 v66, v84, v66
	v_add_f32_e32 v66, v85, v66
	v_add_f32_e32 v66, v86, v66
	v_add_f32_e32 v66, v87, v66
	v_cvt_pk_f16_f32 v102, v82, v83
	v_cvt_pk_f16_f32 v103, v84, v85
	s_nop 0
	ds_read_b64_tr_b16 v[110:111], v156 offset:55296
	ds_read_b64_tr_b16 v[112:113], v156 offset:55808
	s_waitcnt lgkmcnt(14)
	v_mfma_f32_32x32x16_f16 v[34:49], v[164:167], v[136:139], v[34:49]
	v_add_f32_e32 v82, v88, v66
	v_add_f32_e32 v82, v89, v82
	v_add_f32_e32 v82, v90, v82
	v_add_f32_e32 v82, v91, v82
	v_cvt_pk_f16_f32 v104, v86, v87
	v_cvt_pk_f16_f32 v105, v88, v89
	s_nop 0
	ds_read_b64_tr_b16 v[172:173], v156 offset:52224
	ds_read_b64_tr_b16 v[174:175], v156 offset:52736
	s_waitcnt lgkmcnt(14)
	v_mfma_f32_32x32x16_f16 v[50:65], v[168:171], v[132:135], v[50:65]
	v_add_f32_e32 v82, v92, v82
	v_add_f32_e32 v82, v93, v82
	v_add_f32_e32 v82, v94, v82
	v_add_f32_e32 v82, v95, v82
	v_cvt_pk_f16_f32 v98, v90, v91
	v_cvt_pk_f16_f32 v99, v92, v93
	s_nop 0
	ds_read_b64_tr_b16 v[176:177], v156 offset:56320
	ds_read_b64_tr_b16 v[178:179], v156 offset:56832
	v_mfma_f32_32x32x16_f16 v[34:49], v[160:163], v[132:135], v[34:49]
	v_add_f32_e32 v82, v96, v82
	v_add_f32_e32 v82, v97, v82
	v_add_f32_e32 v156, 0, v82
	v_cvt_pk_f16_f32 v100, v94, v95
	v_cvt_pk_f16_f32 v101, v96, v97
	s_nop 0
	s_add_i32 s49, s49, -16
	s_min_i32 s50, s49, s33
	s_cmp_gt_u32 s46, s44
	s_cselect_b64 s[2:3], -1, 0
	s_and_b64 s[48:49], s[2:3], exec
	s_cselect_b32 s48, s50, s46
	s_ashr_i32 s49, s48, 31
	s_lshl_b64 s[48:49], s[48:49], 18
	v_lshl_add_u64 v[82:83], v[194:195], 0, s[48:49]
	s_add_i32 s48, s45, s41
	s_mov_b32 s49, m0
	s_mov_b32 m0, s48
	s_nop 0
	global_load_lds_dwordx4 v[82:83], off
	s_mov_b32 m0, s49
	v_lshl_add_u64 v[82:83], v[82:83], 0, s[22:23]
	s_addk_i32 s48, 0x2000
	s_mov_b32 s49, m0
	s_mov_b32 m0, s48
	s_nop 0
	global_load_lds_dwordx4 v[82:83], off
	s_mov_b32 m0, s49
	v_lshl_add_u64 v[82:83], v[126:127], 0, s[24:25]
	s_add_i32 s48, s43, s40
	s_mov_b32 s49, m0
	s_mov_b32 m0, s48
	s_nop 0
	global_load_lds_dwordx4 v[82:83], off
	s_mov_b32 m0, s49
	v_lshl_add_u64 v[82:83], v[126:127], 0, s[26:27]
	s_addk_i32 s48, 0x2000
	s_mov_b32 s49, m0
	s_mov_b32 m0, s48
	s_nop 0
	global_load_lds_dwordx4 v[82:83], off
	s_mov_b32 m0, s49
	s_andn2_b64 vcc, exec, s[30:31]
	s_mov_b64 s[30:31], -1
	s_cbranch_vccz .LBB1_24
	s_andn2_b64 vcc, exec, s[30:31]
	s_cbranch_vccnz .LBB1_15
.LBB1_13:
	v_max_f32_e64 v82, |v34|, |v34|
	v_max_f32_e64 v83, |v50|, |v50|
	v_min_f32_e32 v82, v83, v82
	v_min3_f32 v82, v82, |v51|, |v35|
	v_min3_f32 v82, v82, |v52|, |v36|
	v_min3_f32 v82, v82, |v53|, |v37|
	v_min3_f32 v82, v82, |v54|, |v38|
	v_min3_f32 v82, v82, |v55|, |v39|
	v_min3_f32 v82, v82, |v56|, |v40|
	v_min3_f32 v82, v82, |v57|, |v41|
	v_min3_f32 v82, v82, |v58|, |v42|
	v_min3_f32 v82, v82, |v59|, |v43|
	v_min3_f32 v82, v82, |v60|, |v44|
	v_min3_f32 v82, v82, |v61|, |v45|
	v_min3_f32 v82, v82, |v62|, |v46|
	v_min3_f32 v82, v82, |v63|, |v47|
	v_min3_f32 v82, v82, |v64|, |v48|
	v_min3_f32 v82, v82, |v65|, |v49|
	v_cmp_eq_f32_e32 vcc, 0, v82
	s_cbranch_vccnz .LBB1_29
.LBB1_14:
.LBB1_15:
	v_max_f32_e32 v66, v51, v51
	v_max_f32_e32 v67, v50, v50
	v_max_f32_e32 v66, v67, v66
	v_max3_f32 v67, v52, v53, v35
	v_max3_f32 v66, v66, v34, v36
	v_max3_f32 v66, v66, v37, v54
	v_max3_f32 v67, v67, v56, v57
	v_max3_f32 v66, v66, v55, v38
	v_max3_f32 v67, v67, v40, v41
	v_max3_f32 v66, v66, v39, v58
	v_max3_f32 v67, v67, v60, v61
	v_max3_f32 v66, v66, v59, v42
	v_max3_f32 v67, v67, v44, v45
	v_max3_f32 v66, v66, v43, v62
	v_max3_f32 v67, v67, v64, v65
	v_max3_f32 v66, v66, v63, v46
	v_max3_f32 v67, v67, v48, v49
	v_max3_f32 v66, v66, v47, v67
	v_mov_b32_e32 v67, v66
	s_nop 1
	v_permlane32_swap_b32_e32 v66, v67
	v_max_f32_e32 v67, v67, v67
	v_max_f32_e32 v66, v66, v66
	v_max_f32_e32 v66, v66, v67
	v_cmp_lt_f32_e32 vcc, s47, v66
	s_cmp_lg_u64 vcc, 0
	v_add_f32_e32 v218, v181, v156
	s_cselect_b64 s[30:31], -1, 0
	s_cbranch_vccnz .LBB1_25

.LBB1_20:
	v_sub_f32_e32 v35, v66, v192
	v_cmp_neq_f32_e32 vcc, 0, v66
	v_sub_f32_e32 v34, v67, v192
	v_pk_add_f32 v[36:37], v[68:69], v[192:193] op_sel_hi:[1,0] neg_lo:[0,1] neg_hi:[0,1]
	v_cndmask_b32_e32 v50, v180, v35, vcc
	v_cmp_neq_f32_e32 vcc, 0, v67
	v_sub_f32_e32 v35, v83, v192
	v_pk_add_f32 v[38:39], v[70:71], v[192:193] op_sel_hi:[1,0] neg_lo:[0,1] neg_hi:[0,1]
	v_cndmask_b32_e32 v51, v180, v34, vcc
	v_sub_f32_e32 v34, v82, v192
	v_cmp_neq_f32_e32 vcc, 0, v82
	v_pk_add_f32 v[40:41], v[72:73], v[192:193] op_sel_hi:[1,0] neg_lo:[0,1] neg_hi:[0,1]
	v_pk_add_f32 v[42:43], v[74:75], v[192:193] op_sel_hi:[1,0] neg_lo:[0,1] neg_hi:[0,1]
	v_cndmask_b32_e32 v34, v180, v34, vcc
	v_cmp_neq_f32_e32 vcc, 0, v83
	v_pk_add_f32 v[44:45], v[76:77], v[192:193] op_sel_hi:[1,0] neg_lo:[0,1] neg_hi:[0,1]
	v_pk_add_f32 v[46:47], v[78:79], v[192:193] op_sel_hi:[1,0] neg_lo:[0,1] neg_hi:[0,1]
	v_cndmask_b32_e32 v35, v180, v35, vcc
	v_cmp_neq_f32_e32 vcc, 0, v68
	v_pk_add_f32 v[48:49], v[80:81], v[192:193] op_sel_hi:[1,0] neg_lo:[0,1] neg_hi:[0,1]
	s_nop 0
	v_cndmask_b32_e32 v52, v180, v36, vcc
	v_cmp_neq_f32_e32 vcc, 0, v69
	s_nop 1
	v_cndmask_b32_e32 v53, v180, v37, vcc
	v_pk_add_f32 v[36:37], v[84:85], v[192:193] op_sel_hi:[1,0] neg_lo:[0,1] neg_hi:[0,1]
	v_cmp_neq_f32_e32 vcc, 0, v84
	s_nop 1
	v_cndmask_b32_e32 v36, v180, v36, vcc
	v_cmp_neq_f32_e32 vcc, 0, v85
	s_nop 1
	v_cndmask_b32_e32 v37, v180, v37, vcc
	v_cmp_neq_f32_e32 vcc, 0, v70
	s_nop 1
	v_cndmask_b32_e32 v54, v180, v38, vcc
	v_cmp_neq_f32_e32 vcc, 0, v71
	s_nop 1
	v_cndmask_b32_e32 v55, v180, v39, vcc
	v_pk_add_f32 v[38:39], v[86:87], v[192:193] op_sel_hi:[1,0] neg_lo:[0,1] neg_hi:[0,1]
	v_cmp_neq_f32_e32 vcc, 0, v86
	s_nop 1
	v_cndmask_b32_e32 v38, v180, v38, vcc
	v_cmp_neq_f32_e32 vcc, 0, v87
	s_nop 1
	v_cndmask_b32_e32 v39, v180, v39, vcc
	v_cmp_neq_f32_e32 vcc, 0, v72
	s_nop 1
	v_cndmask_b32_e32 v56, v180, v40, vcc
	v_cmp_neq_f32_e32 vcc, 0, v73
	s_nop 1
	v_cndmask_b32_e32 v57, v180, v41, vcc
	v_pk_add_f32 v[40:41], v[88:89], v[192:193] op_sel_hi:[1,0] neg_lo:[0,1] neg_hi:[0,1]
	v_cmp_neq_f32_e32 vcc, 0, v88
	s_nop 1
	v_cndmask_b32_e32 v40, v180, v40, vcc
	v_cmp_neq_f32_e32 vcc, 0, v89
	s_nop 1
	v_cndmask_b32_e32 v41, v180, v41, vcc
	v_cmp_neq_f32_e32 vcc, 0, v74
	s_nop 1
	v_cndmask_b32_e32 v58, v180, v42, vcc
	v_cmp_neq_f32_e32 vcc, 0, v75
	s_nop 1
	v_cndmask_b32_e32 v59, v180, v43, vcc
	v_pk_add_f32 v[42:43], v[90:91], v[192:193] op_sel_hi:[1,0] neg_lo:[0,1] neg_hi:[0,1]
	v_cmp_neq_f32_e32 vcc, 0, v90
	s_nop 1
	v_cndmask_b32_e32 v42, v180, v42, vcc
	v_cmp_neq_f32_e32 vcc, 0, v91
	s_nop 1
	v_cndmask_b32_e32 v43, v180, v43, vcc
	v_cmp_neq_f32_e32 vcc, 0, v76
	s_nop 1
	v_cndmask_b32_e32 v60, v180, v44, vcc
	v_cmp_neq_f32_e32 vcc, 0, v77
	s_nop 1
	v_cndmask_b32_e32 v61, v180, v45, vcc
	v_pk_add_f32 v[44:45], v[92:93], v[192:193] op_sel_hi:[1,0] neg_lo:[0,1] neg_hi:[0,1]
	v_cmp_neq_f32_e32 vcc, 0, v92
	s_nop 1
	v_cndmask_b32_e32 v44, v180, v44, vcc
	v_cmp_neq_f32_e32 vcc, 0, v93
	s_nop 1
	v_cndmask_b32_e32 v45, v180, v45, vcc
	v_cmp_neq_f32_e32 vcc, 0, v78
	s_nop 1
	v_cndmask_b32_e32 v62, v180, v46, vcc
	v_cmp_neq_f32_e32 vcc, 0, v79
	s_nop 1
	v_cndmask_b32_e32 v63, v180, v47, vcc
	v_pk_add_f32 v[46:47], v[94:95], v[192:193] op_sel_hi:[1,0] neg_lo:[0,1] neg_hi:[0,1]
	v_cmp_neq_f32_e32 vcc, 0, v94
	s_nop 1
	v_cndmask_b32_e32 v46, v180, v46, vcc
	v_cmp_neq_f32_e32 vcc, 0, v95
	s_nop 1
	v_cndmask_b32_e32 v47, v180, v47, vcc
	v_cmp_neq_f32_e32 vcc, 0, v80
	s_nop 1
	v_cndmask_b32_e32 v64, v180, v48, vcc
	v_cmp_neq_f32_e32 vcc, 0, v81
	s_nop 1
	v_cndmask_b32_e32 v65, v180, v49, vcc
	v_pk_add_f32 v[48:49], v[96:97], v[192:193] op_sel_hi:[1,0] neg_lo:[0,1] neg_hi:[0,1]
	v_cmp_neq_f32_e32 vcc, 0, v96
	s_nop 1
	v_cndmask_b32_e32 v48, v180, v48, vcc
	v_cmp_neq_f32_e32 vcc, 0, v97
	s_nop 1
	v_cndmask_b32_e32 v49, v180, v49, vcc
	v_mov_b32_e32 v82, v34
	v_mov_b32_e32 v83, v35
	v_mov_b32_e32 v84, v36
	v_mov_b32_e32 v85, v37
	v_mov_b32_e32 v86, v38
	v_mov_b32_e32 v87, v39
	v_mov_b32_e32 v88, v40
	v_mov_b32_e32 v89, v41
	v_mov_b32_e32 v90, v42
	v_mov_b32_e32 v91, v43
	v_mov_b32_e32 v92, v44
	v_mov_b32_e32 v93, v45
	v_mov_b32_e32 v94, v46
	v_mov_b32_e32 v95, v47
	v_mov_b32_e32 v96, v48
	v_mov_b32_e32 v97, v49
	v_mov_b32_e32 v66, v50
	v_mov_b32_e32 v67, v51
	v_mov_b32_e32 v68, v52
	v_mov_b32_e32 v69, v53
	v_mov_b32_e32 v70, v54
	v_mov_b32_e32 v71, v55
	v_mov_b32_e32 v72, v56
	v_mov_b32_e32 v73, v57
	v_mov_b32_e32 v74, v58
	v_mov_b32_e32 v75, v59
	v_mov_b32_e32 v76, v60
	v_mov_b32_e32 v77, v61
	v_mov_b32_e32 v78, v62
	v_mov_b32_e32 v79, v63
	v_mov_b32_e32 v80, v64
	v_mov_b32_e32 v81, v65
	s_cbranch_execz .LBB1_6
	s_branch .LBB1_8
.LBB1_21:
	v_max_f32_e32 v50, v50, v50
	v_max_f32_e32 v50, 0, v50
	v_exp_f32_e64 v51, -v50
	s_and_saveexec_b64 s[20:21], s[0:1]
	ds_write_b32 v214, v51
	s_or_b64 exec, exec, s[20:21]
	v_add_f32_e32 v192, v192, v50
	v_mul_f32_e32 v181, v181, v51
	v_pk_add_f32 v[66:67], v[66:67], v[50:51] op_sel_hi:[1,0] neg_lo:[0,1] neg_hi:[0,1]
	v_pk_add_f32 v[82:83], v[82:83], v[50:51] op_sel_hi:[1,0] neg_lo:[0,1] neg_hi:[0,1]
	v_pk_add_f32 v[68:69], v[68:69], v[50:51] op_sel_hi:[1,0] neg_lo:[0,1] neg_hi:[0,1]
	v_pk_add_f32 v[84:85], v[84:85], v[50:51] op_sel_hi:[1,0] neg_lo:[0,1] neg_hi:[0,1]
	v_pk_add_f32 v[70:71], v[70:71], v[50:51] op_sel_hi:[1,0] neg_lo:[0,1] neg_hi:[0,1]
	v_pk_add_f32 v[86:87], v[86:87], v[50:51] op_sel_hi:[1,0] neg_lo:[0,1] neg_hi:[0,1]
	v_pk_add_f32 v[72:73], v[72:73], v[50:51] op_sel_hi:[1,0] neg_lo:[0,1] neg_hi:[0,1]
	v_pk_add_f32 v[88:89], v[88:89], v[50:51] op_sel_hi:[1,0] neg_lo:[0,1] neg_hi:[0,1]
	v_pk_add_f32 v[74:75], v[74:75], v[50:51] op_sel_hi:[1,0] neg_lo:[0,1] neg_hi:[0,1]
	v_pk_add_f32 v[90:91], v[90:91], v[50:51] op_sel_hi:[1,0] neg_lo:[0,1] neg_hi:[0,1]
	v_pk_add_f32 v[76:77], v[76:77], v[50:51] op_sel_hi:[1,0] neg_lo:[0,1] neg_hi:[0,1]
	v_pk_add_f32 v[92:93], v[92:93], v[50:51] op_sel_hi:[1,0] neg_lo:[0,1] neg_hi:[0,1]
	v_pk_add_f32 v[78:79], v[78:79], v[50:51] op_sel_hi:[1,0] neg_lo:[0,1] neg_hi:[0,1]
	v_pk_add_f32 v[94:95], v[94:95], v[50:51] op_sel_hi:[1,0] neg_lo:[0,1] neg_hi:[0,1]
	v_pk_add_f32 v[80:81], v[80:81], v[50:51] op_sel_hi:[1,0] neg_lo:[0,1] neg_hi:[0,1]
	v_pk_add_f32 v[96:97], v[96:97], v[50:51] op_sel_hi:[1,0] neg_lo:[0,1] neg_hi:[0,1]
	s_mov_b64 s[20:21], 0
	s_branch .LBB1_9
.LBB1_24:
	v_sub_f32_e32 v83, v50, v192
	v_cmp_neq_f32_e32 vcc, 0, v50
	v_sub_f32_e32 v82, v51, v192
	v_pk_add_f32 v[84:85], v[52:53], v[192:193] op_sel_hi:[1,0] neg_lo:[0,1] neg_hi:[0,1]
	v_cndmask_b32_e32 v66, v180, v83, vcc
	v_cmp_neq_f32_e32 vcc, 0, v51
	v_sub_f32_e32 v83, v35, v192
	v_pk_add_f32 v[86:87], v[54:55], v[192:193] op_sel_hi:[1,0] neg_lo:[0,1] neg_hi:[0,1]
	v_cndmask_b32_e32 v67, v180, v82, vcc
	v_sub_f32_e32 v82, v34, v192
	v_cmp_neq_f32_e32 vcc, 0, v34
	v_pk_add_f32 v[88:89], v[56:57], v[192:193] op_sel_hi:[1,0] neg_lo:[0,1] neg_hi:[0,1]
	v_pk_add_f32 v[90:91], v[58:59], v[192:193] op_sel_hi:[1,0] neg_lo:[0,1] neg_hi:[0,1]
	v_cndmask_b32_e32 v82, v180, v82, vcc
	v_cmp_neq_f32_e32 vcc, 0, v35
	v_pk_add_f32 v[92:93], v[60:61], v[192:193] op_sel_hi:[1,0] neg_lo:[0,1] neg_hi:[0,1]
	v_pk_add_f32 v[94:95], v[62:63], v[192:193] op_sel_hi:[1,0] neg_lo:[0,1] neg_hi:[0,1]
	v_cndmask_b32_e32 v83, v180, v83, vcc
	v_cmp_neq_f32_e32 vcc, 0, v52
	v_pk_add_f32 v[96:97], v[64:65], v[192:193] op_sel_hi:[1,0] neg_lo:[0,1] neg_hi:[0,1]
	s_nop 0
	v_cndmask_b32_e32 v68, v180, v84, vcc
	v_cmp_neq_f32_e32 vcc, 0, v53
	s_nop 1
	v_cndmask_b32_e32 v69, v180, v85, vcc
	v_pk_add_f32 v[84:85], v[36:37], v[192:193] op_sel_hi:[1,0] neg_lo:[0,1] neg_hi:[0,1]
	v_cmp_neq_f32_e32 vcc, 0, v36
	s_nop 1
	v_cndmask_b32_e32 v84, v180, v84, vcc
	v_cmp_neq_f32_e32 vcc, 0, v37
	s_nop 1
	v_cndmask_b32_e32 v85, v180, v85, vcc
	v_cmp_neq_f32_e32 vcc, 0, v54
	s_nop 1
	v_cndmask_b32_e32 v70, v180, v86, vcc
	v_cmp_neq_f32_e32 vcc, 0, v55
	s_nop 1
	v_cndmask_b32_e32 v71, v180, v87, vcc
	v_pk_add_f32 v[86:87], v[38:39], v[192:193] op_sel_hi:[1,0] neg_lo:[0,1] neg_hi:[0,1]
	v_cmp_neq_f32_e32 vcc, 0, v38
	s_nop 1
	v_cndmask_b32_e32 v86, v180, v86, vcc
	v_cmp_neq_f32_e32 vcc, 0, v39
	s_nop 1
	v_cndmask_b32_e32 v87, v180, v87, vcc
	v_cmp_neq_f32_e32 vcc, 0, v56
	s_nop 1
	v_cndmask_b32_e32 v72, v180, v88, vcc
	v_cmp_neq_f32_e32 vcc, 0, v57
	s_nop 1
	v_cndmask_b32_e32 v73, v180, v89, vcc
	v_pk_add_f32 v[88:89], v[40:41], v[192:193] op_sel_hi:[1,0] neg_lo:[0,1] neg_hi:[0,1]
	v_cmp_neq_f32_e32 vcc, 0, v40
	s_nop 1
	v_cndmask_b32_e32 v88, v180, v88, vcc
	v_cmp_neq_f32_e32 vcc, 0, v41
	s_nop 1
	v_cndmask_b32_e32 v89, v180, v89, vcc
	v_cmp_neq_f32_e32 vcc, 0, v58
	s_nop 1
	v_cndmask_b32_e32 v74, v180, v90, vcc
	v_cmp_neq_f32_e32 vcc, 0, v59
	s_nop 1
	v_cndmask_b32_e32 v75, v180, v91, vcc
	v_pk_add_f32 v[90:91], v[42:43], v[192:193] op_sel_hi:[1,0] neg_lo:[0,1] neg_hi:[0,1]
	v_cmp_neq_f32_e32 vcc, 0, v42
	s_nop 1
	v_cndmask_b32_e32 v90, v180, v90, vcc
	v_cmp_neq_f32_e32 vcc, 0, v43
	s_nop 1
	v_cndmask_b32_e32 v91, v180, v91, vcc
	v_cmp_neq_f32_e32 vcc, 0, v60
	s_nop 1
	v_cndmask_b32_e32 v76, v180, v92, vcc
	v_cmp_neq_f32_e32 vcc, 0, v61
	s_nop 1
	v_cndmask_b32_e32 v77, v180, v93, vcc
	v_pk_add_f32 v[92:93], v[44:45], v[192:193] op_sel_hi:[1,0] neg_lo:[0,1] neg_hi:[0,1]
	v_cmp_neq_f32_e32 vcc, 0, v44
	s_nop 1
	v_cndmask_b32_e32 v92, v180, v92, vcc
	v_cmp_neq_f32_e32 vcc, 0, v45
	s_nop 1
	v_cndmask_b32_e32 v93, v180, v93, vcc
	v_cmp_neq_f32_e32 vcc, 0, v62
	s_nop 1
	v_cndmask_b32_e32 v78, v180, v94, vcc
	v_cmp_neq_f32_e32 vcc, 0, v63
	s_nop 1
	v_cndmask_b32_e32 v79, v180, v95, vcc
	v_pk_add_f32 v[94:95], v[46:47], v[192:193] op_sel_hi:[1,0] neg_lo:[0,1] neg_hi:[0,1]
	v_cmp_neq_f32_e32 vcc, 0, v46
	s_nop 1
	v_cndmask_b32_e32 v94, v180, v94, vcc
	v_cmp_neq_f32_e32 vcc, 0, v47
	s_nop 1
	v_cndmask_b32_e32 v95, v180, v95, vcc
	v_cmp_neq_f32_e32 vcc, 0, v64
	s_nop 1
	v_cndmask_b32_e32 v80, v180, v96, vcc
	v_cmp_neq_f32_e32 vcc, 0, v65
	s_nop 1
	v_cndmask_b32_e32 v81, v180, v97, vcc
	v_pk_add_f32 v[96:97], v[48:49], v[192:193] op_sel_hi:[1,0] neg_lo:[0,1] neg_hi:[0,1]
	v_cmp_neq_f32_e32 vcc, 0, v48
	s_nop 1
	v_cndmask_b32_e32 v96, v180, v96, vcc
	v_cmp_neq_f32_e32 vcc, 0, v49
	s_nop 1
	v_cndmask_b32_e32 v97, v180, v97, vcc
	v_mov_b32_e32 v34, v82
	v_mov_b32_e32 v35, v83
	v_mov_b32_e32 v36, v84
	v_mov_b32_e32 v37, v85
	v_mov_b32_e32 v38, v86
	v_mov_b32_e32 v39, v87
	v_mov_b32_e32 v40, v88
	v_mov_b32_e32 v41, v89
	v_mov_b32_e32 v42, v90
	v_mov_b32_e32 v43, v91
	v_mov_b32_e32 v44, v92
	v_mov_b32_e32 v45, v93
	v_mov_b32_e32 v46, v94
	v_mov_b32_e32 v47, v95
	v_mov_b32_e32 v48, v96
	v_mov_b32_e32 v49, v97
	v_mov_b32_e32 v50, v66
	v_mov_b32_e32 v51, v67
	v_mov_b32_e32 v52, v68
	v_mov_b32_e32 v53, v69
	v_mov_b32_e32 v54, v70
	v_mov_b32_e32 v55, v71
	v_mov_b32_e32 v56, v72
	v_mov_b32_e32 v57, v73
	v_mov_b32_e32 v58, v74
	v_mov_b32_e32 v59, v75
	v_mov_b32_e32 v60, v76
	v_mov_b32_e32 v61, v77
	v_mov_b32_e32 v62, v78
	v_mov_b32_e32 v63, v79
	v_mov_b32_e32 v64, v80
	v_mov_b32_e32 v65, v81
	s_cbranch_execz .LBB1_13
	s_branch .LBB1_15

.LBB1_29:
	v_cmp_neq_f32_e32 vcc, 0, v50
	s_nop 1
	v_cndmask_b32_e32 v50, v180, v50, vcc
	v_cmp_neq_f32_e32 vcc, 0, v34
	s_nop 1
	v_cndmask_b32_e32 v34, v180, v34, vcc
	v_cmp_neq_f32_e32 vcc, 0, v51
	s_nop 1
	v_cndmask_b32_e32 v51, v180, v51, vcc
	v_cmp_neq_f32_e32 vcc, 0, v35
	s_nop 1
	v_cndmask_b32_e32 v35, v180, v35, vcc
	v_cmp_neq_f32_e32 vcc, 0, v52
	s_nop 1
	v_cndmask_b32_e32 v52, v180, v52, vcc
	v_cmp_neq_f32_e32 vcc, 0, v36
	s_nop 1
	v_cndmask_b32_e32 v36, v180, v36, vcc
	v_cmp_neq_f32_e32 vcc, 0, v53
	s_nop 1
	v_cndmask_b32_e32 v53, v180, v53, vcc
	v_cmp_neq_f32_e32 vcc, 0, v37
	s_nop 1
	v_cndmask_b32_e32 v37, v180, v37, vcc
	v_cmp_neq_f32_e32 vcc, 0, v54
	s_nop 1
	v_cndmask_b32_e32 v54, v180, v54, vcc
	v_cmp_neq_f32_e32 vcc, 0, v38
	s_nop 1
	v_cndmask_b32_e32 v38, v180, v38, vcc
	v_cmp_neq_f32_e32 vcc, 0, v55
	s_nop 1
	v_cndmask_b32_e32 v55, v180, v55, vcc
	v_cmp_neq_f32_e32 vcc, 0, v39
	s_nop 1
	v_cndmask_b32_e32 v39, v180, v39, vcc
	v_cmp_neq_f32_e32 vcc, 0, v56
	s_nop 1
	v_cndmask_b32_e32 v56, v180, v56, vcc
	v_cmp_neq_f32_e32 vcc, 0, v40
	s_nop 1
	v_cndmask_b32_e32 v40, v180, v40, vcc
	v_cmp_neq_f32_e32 vcc, 0, v57
	s_nop 1
	v_cndmask_b32_e32 v57, v180, v57, vcc
	v_cmp_neq_f32_e32 vcc, 0, v41
	s_nop 1
	v_cndmask_b32_e32 v41, v180, v41, vcc
	v_cmp_neq_f32_e32 vcc, 0, v58
	s_nop 1
	v_cndmask_b32_e32 v58, v180, v58, vcc
	v_cmp_neq_f32_e32 vcc, 0, v42
	s_nop 1
	v_cndmask_b32_e32 v42, v180, v42, vcc
	v_cmp_neq_f32_e32 vcc, 0, v59
	s_nop 1
	v_cndmask_b32_e32 v59, v180, v59, vcc
	v_cmp_neq_f32_e32 vcc, 0, v43
	s_nop 1
	v_cndmask_b32_e32 v43, v180, v43, vcc
	v_cmp_neq_f32_e32 vcc, 0, v60
	s_nop 1
	v_cndmask_b32_e32 v60, v180, v60, vcc
	v_cmp_neq_f32_e32 vcc, 0, v44
	s_nop 1
	v_cndmask_b32_e32 v44, v180, v44, vcc
	v_cmp_neq_f32_e32 vcc, 0, v61
	s_nop 1
	v_cndmask_b32_e32 v61, v180, v61, vcc
	v_cmp_neq_f32_e32 vcc, 0, v45
	s_nop 1
	v_cndmask_b32_e32 v45, v180, v45, vcc
	v_cmp_neq_f32_e32 vcc, 0, v62
	s_nop 1
	v_cndmask_b32_e32 v62, v180, v62, vcc
	v_cmp_neq_f32_e32 vcc, 0, v46
	s_nop 1
	v_cndmask_b32_e32 v46, v180, v46, vcc
	v_cmp_neq_f32_e32 vcc, 0, v63
	s_nop 1
	v_cndmask_b32_e32 v63, v180, v63, vcc
	v_cmp_neq_f32_e32 vcc, 0, v47
	s_nop 1
	v_cndmask_b32_e32 v47, v180, v47, vcc
	v_cmp_neq_f32_e32 vcc, 0, v64
	s_nop 1
	v_cndmask_b32_e32 v64, v180, v64, vcc
	v_cmp_neq_f32_e32 vcc, 0, v48
	s_nop 1
	v_cndmask_b32_e32 v48, v180, v48, vcc
	v_cmp_neq_f32_e32 vcc, 0, v65
	s_nop 1
	v_cndmask_b32_e32 v65, v180, v65, vcc
	v_cmp_neq_f32_e32 vcc, 0, v49
	s_nop 1
	v_cndmask_b32_e32 v49, v180, v49, vcc
	s_branch .LBB1_14

.LBB1_135:
	v_mov_b32_e32 v32, 0xff800000
	v_cmp_neq_f32_e32 vcc, 0, v80
	s_nop 1
	v_cndmask_b32_e32 v80, v32, v80, vcc
	v_cmp_neq_f32_e32 vcc, 0, v96
	s_nop 1
	v_cndmask_b32_e32 v96, v32, v96, vcc
	v_cmp_neq_f32_e32 vcc, 0, v81
	s_nop 1
	v_cndmask_b32_e32 v81, v32, v81, vcc
	v_cmp_neq_f32_e32 vcc, 0, v97
	s_nop 1
	v_cndmask_b32_e32 v97, v32, v97, vcc
	v_cmp_neq_f32_e32 vcc, 0, v82
	s_nop 1
	v_cndmask_b32_e32 v82, v32, v82, vcc
	v_cmp_neq_f32_e32 vcc, 0, v98
	s_nop 1
	v_cndmask_b32_e32 v98, v32, v98, vcc
	v_cmp_neq_f32_e32 vcc, 0, v83
	s_nop 1
	v_cndmask_b32_e32 v83, v32, v83, vcc
	v_cmp_neq_f32_e32 vcc, 0, v99
	s_nop 1
	v_cndmask_b32_e32 v99, v32, v99, vcc
	v_cmp_neq_f32_e32 vcc, 0, v84
	s_nop 1
	v_cndmask_b32_e32 v84, v32, v84, vcc
	v_cmp_neq_f32_e32 vcc, 0, v100
	s_nop 1
	v_cndmask_b32_e32 v100, v32, v100, vcc
	v_cmp_neq_f32_e32 vcc, 0, v85
	s_nop 1
	v_cndmask_b32_e32 v85, v32, v85, vcc
	v_cmp_neq_f32_e32 vcc, 0, v101
	s_nop 1
	v_cndmask_b32_e32 v101, v32, v101, vcc
	v_cmp_neq_f32_e32 vcc, 0, v86
	s_nop 1
	v_cndmask_b32_e32 v86, v32, v86, vcc
	v_cmp_neq_f32_e32 vcc, 0, v102
	s_nop 1
	v_cndmask_b32_e32 v102, v32, v102, vcc
	v_cmp_neq_f32_e32 vcc, 0, v87
	s_nop 1
	v_cndmask_b32_e32 v87, v32, v87, vcc
	v_cmp_neq_f32_e32 vcc, 0, v103
	s_nop 1
	v_cndmask_b32_e32 v103, v32, v103, vcc
	v_cmp_neq_f32_e32 vcc, 0, v88
	s_nop 1
	v_cndmask_b32_e32 v88, v32, v88, vcc
	v_cmp_neq_f32_e32 vcc, 0, v104
	s_nop 1
	v_cndmask_b32_e32 v104, v32, v104, vcc
	v_cmp_neq_f32_e32 vcc, 0, v89
	s_nop 1
	v_cndmask_b32_e32 v89, v32, v89, vcc
	v_cmp_neq_f32_e32 vcc, 0, v105
	s_nop 1
	v_cndmask_b32_e32 v105, v32, v105, vcc
	v_cmp_neq_f32_e32 vcc, 0, v90
	s_nop 1
	v_cndmask_b32_e32 v90, v32, v90, vcc
	v_cmp_neq_f32_e32 vcc, 0, v106
	s_nop 1
	v_cndmask_b32_e32 v106, v32, v106, vcc
	v_cmp_neq_f32_e32 vcc, 0, v91
	s_nop 1
	v_cndmask_b32_e32 v91, v32, v91, vcc
	v_cmp_neq_f32_e32 vcc, 0, v107
	s_nop 1
	v_cndmask_b32_e32 v107, v32, v107, vcc
	v_cmp_neq_f32_e32 vcc, 0, v92
	s_nop 1
	v_cndmask_b32_e32 v92, v32, v92, vcc
	v_cmp_neq_f32_e32 vcc, 0, v108
	s_nop 1
	v_cndmask_b32_e32 v108, v32, v108, vcc
	v_cmp_neq_f32_e32 vcc, 0, v93
	s_nop 1
	v_cndmask_b32_e32 v93, v32, v93, vcc
	v_cmp_neq_f32_e32 vcc, 0, v109
	s_nop 1
	v_cndmask_b32_e32 v109, v32, v109, vcc
	v_cmp_neq_f32_e32 vcc, 0, v94
	s_nop 1
	v_cndmask_b32_e32 v94, v32, v94, vcc
	v_cmp_neq_f32_e32 vcc, 0, v110
	s_nop 1
	v_cndmask_b32_e32 v110, v32, v110, vcc
	v_cmp_neq_f32_e32 vcc, 0, v95
	s_nop 1
	v_cndmask_b32_e32 v95, v32, v95, vcc
	v_cmp_neq_f32_e32 vcc, 0, v111
	s_nop 1
	v_cndmask_b32_e32 v111, v32, v111, vcc
	s_branch .LBB1_93
	s_nop 0
	s_nop 0
	s_nop 0
	s_nop 0
	s_nop 0
	s_nop 0
	s_nop 0
	s_nop 0
	s_nop 0
	s_nop 0
	s_nop 0
	s_nop 0
	s_nop 0
	s_nop 0
	s_nop 0
	s_nop 0
	s_nop 0
	s_nop 0
	s_nop 0
	s_nop 0
	s_nop 0
	s_nop 0
	s_nop 0
	s_nop 0
	s_nop 0
	s_nop 0
	s_nop 0
	s_nop 0
	s_nop 0
	s_nop 0
	s_nop 0
	s_nop 0
	s_nop 0
	s_nop 0
	s_nop 0
	s_endpgm

.LBB2_2:
	s_load_dword s3, s[0:1], 0x20
	s_load_dwordx2 s[8:9], s[0:1], 0x10
	s_and_b32 s10, s2, 7
	v_cvt_f32_ubyte0_e32 v3, s10
	v_lshrrev_b32_e32 v12, 4, v0
	s_waitcnt lgkmcnt(0)
	s_mul_hi_i32 s0, s3, 0x2aaaaaab
	s_lshr_b32 s1, s0, 31
	s_ashr_i32 s0, s0, 7
	s_add_i32 s3, s0, s1
	v_cvt_f32_i32_e32 v1, s3
	s_ashr_i32 s0, s3, 30
	s_or_b32 s11, s0, 1
	v_xor_b32_e32 v10, v12, v0
	v_rcp_iflag_f32_e32 v2, v1
	v_lshlrev_b32_e32 v149, 4, v0
	v_mov_b32_e32 v11, 0x60
	v_add_u32_e32 v14, 0, v149
	v_mul_f32_e32 v2, v3, v2
	v_trunc_f32_e32 v2, v2
	v_fma_f32 v3, -v2, v1, v3
	v_cvt_i32_f32_e32 v2, v2
	v_cmp_ge_f32_e64 s[0:1], |v3|, |v1|
	s_and_b64 s[0:1], s[0:1], exec
	s_cselect_b32 s0, s11, 0
	v_readfirstlane_b32 s1, v2
	s_add_i32 s1, s1, s0
	s_bfe_i32 s0, s1, 0x170000
	s_mul_i32 s0, s0, s3
	s_sub_i32 s0, s10, s0
	s_lshl_b32 s0, s0, 2
	s_lshr_b32 s3, s2, 6
	s_add_i32 s13, s0, s3
	s_lshl_b32 s0, s2, 5
	s_lshl_b32 s15, s1, 11
	s_and_b32 s18, s0, 0x700
	s_or_b32 s12, s15, s18
	v_lshrrev_b32_e32 v1, 3, v0
	v_or_b32_e32 v2, s12, v1
	s_mulk_i32 s13, 0xc0
	v_ashrrev_i32_e32 v3, 31, v2
	v_lshlrev_b64 v[4:5], 11, v[2:3]
	v_or_b32_e32 v2, s13, v1
	v_mov_b32_e32 v3, 0
	v_lshlrev_b64 v[6:7], 11, v[2:3]
	v_lshlrev_b32_e32 v2, 4, v10
	v_and_b32_e32 v10, 64, v0
	v_cmp_ne_u32_e32 vcc, 0, v10
	v_and_b32_e32 v143, 15, v0
	v_lshl_add_u64 v[4:5], s[4:5], 0, v[4:5]
	v_and_b32_e32 v2, 0x70, v2
	v_cndmask_b32_e32 v142, 0, v11, vcc
	v_readfirstlane_b32 s0, v14
	v_add_u32_e32 v16, 0x2000, v14
	v_lshl_add_u64 v[4:5], v[4:5], 0, v[2:3]
	v_or_b32_e32 v10, v142, v143
	s_mov_b32 m0, s0
	s_mov_b64 s[0:1], 0x20000
	v_readfirstlane_b32 s2, v16
	v_add_u32_e32 v16, 0x4000, v14
	v_lshlrev_b32_e32 v146, 7, v10
	global_load_lds_dwordx4 v[4:5], off
	v_lshl_add_u64 v[10:11], v[4:5], 0, s[0:1]
	s_mov_b32 m0, s2
	s_mov_b64 s[2:3], 0x40000
	v_readfirstlane_b32 s10, v16
	global_load_lds_dwordx4 v[10:11], off
	v_lshl_add_u64 v[10:11], v[4:5], 0, s[2:3]
	s_mov_b32 m0, s10
	s_mov_b64 s[10:11], 0x60000
	v_add_u32_e32 v16, 0x6000, v14
	v_lshl_add_u64 v[8:9], s[6:7], 0, v[6:7]
	v_add_u32_e32 v15, 0x8000, v14
	global_load_lds_dwordx4 v[10:11], off
	v_lshl_add_u64 v[10:11], v[4:5], 0, s[10:11]
	v_readfirstlane_b32 s10, v16
	v_lshl_add_u64 v[8:9], v[8:9], 0, v[2:3]
	s_mov_b32 m0, s10
	v_readfirstlane_b32 s10, v15
	v_add_u32_e32 v15, 0xa000, v14
	v_lshrrev_b32_e32 v2, 1, v0
	global_load_lds_dwordx4 v[10:11], off
	s_mov_b32 m0, s10
	v_lshl_add_u64 v[10:11], v[8:9], 0, s[0:1]
	v_readfirstlane_b32 s0, v15
	v_add_u32_e32 v15, 0xc000, v14
	v_bfe_u32 v145, v0, 4, 2
	v_and_b32_e32 v141, 0xc0, v2
	global_load_lds_dwordx4 v[8:9], off
	s_mov_b32 m0, s0
	v_readfirstlane_b32 s0, v15
	v_bitop3_b32 v13, v145, v2, 7 bitop3:0x78
	v_or_b32_e32 v2, v141, v143
	global_load_lds_dwordx4 v[10:11], off
	s_mov_b32 m0, s0
	s_add_i32 s0, 0, 0x16000
	v_add_u32_e32 v15, 0xe000, v14
	v_lshl_add_u64 v[10:11], v[8:9], 0, s[2:3]
	v_lshlrev_b32_e32 v147, 7, v2
	v_add_u32_e32 v2, s0, v149
	s_mov_b64 s[0:1], 0x80
	v_readfirstlane_b32 s2, v15
	v_add_u32_e32 v15, 0x10000, v14
	global_load_lds_dwordx4 v[10:11], off
	v_lshl_add_u64 v[10:11], v[4:5], 0, s[0:1]
	s_mov_b32 m0, s2
	s_mov_b64 s[2:3], 0x20080
	v_readfirstlane_b32 s10, v15
	v_add_u32_e32 v15, 0x12000, v14
	global_load_lds_dwordx4 v[10:11], off
	v_lshl_add_u64 v[10:11], v[4:5], 0, s[2:3]
	s_mov_b32 m0, s10
	s_mov_b64 s[10:11], 0x40080
	v_readfirstlane_b32 s16, v15
	global_load_lds_dwordx4 v[10:11], off
	v_lshl_add_u64 v[10:11], v[4:5], 0, s[10:11]
	s_mov_b32 m0, s16
	s_mov_b64 s[16:17], 0x60080
	global_load_lds_dwordx4 v[10:11], off
	v_add_u32_e32 v10, 0x14000, v14
	v_lshl_add_u64 v[4:5], v[4:5], 0, s[16:17]
	v_readfirstlane_b32 s16, v10
	s_mov_b32 m0, s16
	v_add_u32_e32 v10, 0x2000, v2
	global_load_lds_dwordx4 v[4:5], off
	v_lshl_add_u64 v[4:5], v[8:9], 0, s[0:1]
	v_readfirstlane_b32 s0, v2
	s_mov_b32 m0, s0
	v_readfirstlane_b32 s0, v10
	v_add_u32_e32 v2, 0x4000, v2
	global_load_lds_dwordx4 v[4:5], off
	v_lshl_add_u64 v[4:5], v[8:9], 0, s[2:3]
	s_mov_b32 m0, s0
	v_readfirstlane_b32 s0, v2
	global_load_lds_dwordx4 v[4:5], off
	v_lshl_add_u64 v[4:5], v[8:9], 0, s[10:11]
	s_mov_b32 m0, s0
	v_lshlrev_b32_e32 v2, 4, v13
	global_load_lds_dwordx4 v[4:5], off
	s_waitcnt vmcnt(7) lgkmcnt(0)
	s_barrier
	v_add3_u32 v150, 0, v147, v2
	v_add3_u32 v151, 0, v146, v2
	ds_read_b128 v[118:121], v150
	ds_read_b128 v[106:109], v150 offset:2048
	ds_read_b128 v[86:89], v150 offset:4096
	ds_read_b128 v[34:37], v150 offset:6144
	ds_read_b128 v[98:101], v151 offset:32768
	ds_read_b128 v[90:93], v151 offset:34816
	ds_read_b128 v[82:85], v151 offset:36864
	ds_read_b128 v[74:77], v151 offset:38912
	ds_read_b128 v[66:69], v151 offset:40960
	ds_read_b128 v[50:53], v151 offset:43008
	v_or_b32_e32 v1, s15, v1
	v_or_b32_e32 v4, s18, v1
	v_and_b32_e32 v140, 63, v0
	v_lshrrev_b32_e32 v144, 6, v0
	v_ashrrev_i32_e32 v5, 31, v4
	v_bitop3_b32 v0, v12, 7, v0 bitop3:0x48
	v_xor_b32_e32 v148, 64, v2
	v_lshlrev_b64 v[4:5], 11, v[4:5]
	v_lshlrev_b32_e32 v2, 4, v0
	v_or_b32_e32 v4, v4, v2
	v_or_b32_e32 v6, v6, v2
	s_mov_b32 s14, 0
	v_lshl_add_u64 v[0:1], s[4:5], 0, v[4:5]
	v_lshl_add_u64 v[138:139], s[6:7], 0, v[6:7]
	s_mov_b64 s[0:1], 0
	s_mov_b64 s[2:3], 0x100
	s_mov_b64 s[4:5], 0x20100
	s_mov_b64 s[6:7], 0x40100
	s_mov_b64 s[10:11], 0x60100
	v_lshl_add_u64 v[192:193], v[0:1], 0, s[2:3]
	v_lshl_add_u64 v[194:195], v[0:1], 0, s[4:5]
	v_lshl_add_u64 v[196:197], v[0:1], 0, s[6:7]
	v_lshl_add_u64 v[198:199], v[0:1], 0, s[10:11]
	v_lshl_add_u64 v[200:201], v[138:139], 0, s[2:3]
	v_lshl_add_u64 v[202:203], v[138:139], 0, s[4:5]
	v_lshl_add_u64 v[204:205], v[138:139], 0, s[6:7]
	v_readfirstlane_b32 s21, v149
	s_mov_b64 s[22:23], 0x80
	v_mov_b32_e32 v2, v3
	v_mov_b32_e32 v4, v3
	v_mov_b32_e32 v5, v3
	v_mov_b32_e32 v6, v3
	v_mov_b32_e32 v7, v3
	v_mov_b32_e32 v8, v3
	v_mov_b32_e32 v9, v3
	v_mov_b32_e32 v10, v3
	v_mov_b32_e32 v11, v3
	v_mov_b32_e32 v12, v3
	v_mov_b32_e32 v13, v3
	v_mov_b32_e32 v14, v3
	v_mov_b32_e32 v15, v3
	v_mov_b32_e32 v16, v3
	v_mov_b32_e32 v17, v3
	v_mov_b32_e32 v18, v3
	v_mov_b32_e32 v19, v3
	v_mov_b32_e32 v20, v3
	v_mov_b32_e32 v21, v3
	v_mov_b32_e32 v22, v3
	v_mov_b32_e32 v23, v3
	v_mov_b32_e32 v24, v3
	v_mov_b32_e32 v25, v3
	v_mov_b32_e32 v26, v3
	v_mov_b32_e32 v27, v3
	v_mov_b32_e32 v28, v3
	v_mov_b32_e32 v29, v3
	v_mov_b32_e32 v30, v3
	v_mov_b32_e32 v31, v3
	v_mov_b32_e32 v32, v3
	v_mov_b32_e32 v33, v3
	v_mov_b32_e32 v38, v3
	v_mov_b32_e32 v39, v3
	v_mov_b32_e32 v40, v3
	v_mov_b32_e32 v41, v3
	v_mov_b32_e32 v42, v3
	v_mov_b32_e32 v43, v3
	v_mov_b32_e32 v44, v3
	v_mov_b32_e32 v45, v3
	v_mov_b32_e32 v46, v3
	v_mov_b32_e32 v47, v3
	v_mov_b32_e32 v48, v3
	v_mov_b32_e32 v49, v3
	v_mov_b32_e32 v54, v3
	v_mov_b32_e32 v55, v3
	v_mov_b32_e32 v56, v3
	v_mov_b32_e32 v57, v3
	v_mov_b32_e32 v58, v3
	v_mov_b32_e32 v59, v3
	v_mov_b32_e32 v60, v3
	v_mov_b32_e32 v61, v3
	v_mov_b32_e32 v62, v3
	v_mov_b32_e32 v63, v3
	v_mov_b32_e32 v64, v3
	v_mov_b32_e32 v65, v3
	v_mov_b32_e32 v70, v3
	v_mov_b32_e32 v71, v3
	v_mov_b32_e32 v72, v3
	v_mov_b32_e32 v73, v3
	v_mov_b32_e32 v78, v3
	v_mov_b32_e32 v79, v3
	v_mov_b32_e32 v80, v3
	v_mov_b32_e32 v81, v3
	v_mov_b32_e32 v94, v3
	v_mov_b32_e32 v95, v3
	v_mov_b32_e32 v96, v3
	v_mov_b32_e32 v97, v3
	v_mov_b32_e32 v102, v3
	v_mov_b32_e32 v103, v3
	v_mov_b32_e32 v104, v3
	v_mov_b32_e32 v105, v3
	v_mov_b32_e32 v110, v3
	v_mov_b32_e32 v111, v3
	v_mov_b32_e32 v112, v3
	v_mov_b32_e32 v113, v3
	v_mov_b32_e32 v114, v3
	v_mov_b32_e32 v115, v3
	v_mov_b32_e32 v116, v3
	v_mov_b32_e32 v117, v3
	v_mov_b32_e32 v122, v3
	v_mov_b32_e32 v123, v3
	v_mov_b32_e32 v124, v3
	v_mov_b32_e32 v125, v3
	v_mov_b32_e32 v126, v3
	v_mov_b32_e32 v127, v3
	v_mov_b32_e32 v128, v3
	v_mov_b32_e32 v129, v3
	v_mov_b32_e32 v130, v3
	v_mov_b32_e32 v131, v3
	v_mov_b32_e32 v132, v3
	v_mov_b32_e32 v133, v3
	v_mov_b32_e32 v134, v3
	v_mov_b32_e32 v135, v3
	v_mov_b32_e32 v136, v3
	v_mov_b32_e32 v137, v3
.LBB2_3:
	s_mul_i32 s15, s14, 0xe000
	s_add_i32 s14, s14, 1
	s_cmp_lg_u32 s14, 2
	s_cselect_b32 s14, s14, 0
	s_add_i32 s20, s15, s21
	v_add3_u32 v206, s15, v147, v148
	v_add3_u32 v207, s15, v146, v148
	s_waitcnt lgkmcnt(8)
	v_mfma_f32_16x16x32_f16 v[134:137], v[98:101], v[118:121], v[134:137]
	s_waitcnt lgkmcnt(7)
	v_mfma_f32_16x16x32_f16 v[130:133], v[90:93], v[118:121], v[130:133]
	s_waitcnt lgkmcnt(6)
	v_mfma_f32_16x16x32_f16 v[102:105], v[98:101], v[106:109], v[102:105]
	ds_read_b128 v[152:155], v206
	v_mfma_f32_16x16x32_f16 v[94:97], v[90:93], v[106:109], v[94:97]
	ds_read_b128 v[168:171], v207 offset:32768
	s_waitcnt lgkmcnt(7)
	v_mfma_f32_16x16x32_f16 v[126:129], v[82:85], v[118:121], v[126:129]
	ds_read_b128 v[172:175], v207 offset:34816
	v_mfma_f32_16x16x32_f16 v[78:81], v[82:85], v[106:109], v[78:81]
	ds_read_b128 v[156:159], v206 offset:2048
	s_waitcnt lgkmcnt(8)
	v_mfma_f32_16x16x32_f16 v[122:125], v[74:77], v[118:121], v[122:125]
	ds_read_b128 v[176:179], v207 offset:36864
	v_mfma_f32_16x16x32_f16 v[70:73], v[74:77], v[106:109], v[70:73]
	ds_read_b128 v[180:183], v207 offset:38912
	s_waitcnt lgkmcnt(9)
	v_mfma_f32_16x16x32_f16 v[54:57], v[98:101], v[86:89], v[54:57]
	ds_read_b128 v[160:163], v206 offset:4096
	v_mfma_f32_16x16x32_f16 v[46:49], v[90:93], v[86:89], v[46:49]
	ds_read_b128 v[184:187], v207 offset:40960
	v_mfma_f32_16x16x32_f16 v[42:45], v[82:85], v[86:89], v[42:45]
	ds_read_b128 v[188:191], v207 offset:43008
	v_mfma_f32_16x16x32_f16 v[38:41], v[74:77], v[86:89], v[38:41]
	ds_read_b128 v[164:167], v206 offset:6144
	s_waitcnt lgkmcnt(12)
	v_mfma_f32_16x16x32_f16 v[114:117], v[66:69], v[118:121], v[114:117]
	v_mfma_f32_16x16x32_f16 v[62:65], v[66:69], v[106:109], v[62:65]
	v_mfma_f32_16x16x32_f16 v[30:33], v[66:69], v[86:89], v[30:33]
	s_waitcnt lgkmcnt(11)
	v_mfma_f32_16x16x32_f16 v[110:113], v[50:53], v[118:121], v[110:113]
	v_mfma_f32_16x16x32_f16 v[58:61], v[50:53], v[106:109], v[58:61]
	v_mfma_f32_16x16x32_f16 v[26:29], v[50:53], v[86:89], v[26:29]
	s_waitcnt lgkmcnt(10)
	v_mfma_f32_16x16x32_f16 v[22:25], v[98:101], v[34:37], v[22:25]
	v_mfma_f32_16x16x32_f16 v[18:21], v[90:93], v[34:37], v[18:21]
	v_mfma_f32_16x16x32_f16 v[14:17], v[82:85], v[34:37], v[14:17]
	v_mfma_f32_16x16x32_f16 v[10:13], v[74:77], v[34:37], v[10:13]
	v_mfma_f32_16x16x32_f16 v[6:9], v[66:69], v[34:37], v[6:9]
	v_mfma_f32_16x16x32_f16 v[2:5], v[50:53], v[34:37], v[2:5]
	s_waitcnt vmcnt(0) lgkmcnt(0)
	s_barrier
	s_mov_b32 m0, s20
	s_mul_i32 s15, s14, 0xe000
	v_mfma_f32_16x16x32_f16 v[134:137], v[168:171], v[152:155], v[134:137]
	global_load_lds_dwordx4 v[192:193], off
	v_lshl_add_u64 v[192:193], v[192:193], 0, s[22:23]
	s_add_u32 m0, s20, 0x2000
	v_mfma_f32_16x16x32_f16 v[130:133], v[172:175], v[152:155], v[130:133]
	v_mfma_f32_16x16x32_f16 v[126:129], v[176:179], v[152:155], v[126:129]
	global_load_lds_dwordx4 v[194:195], off
	v_lshl_add_u64 v[194:195], v[194:195], 0, s[22:23]
	s_add_u32 m0, s20, 0x4000
	v_mfma_f32_16x16x32_f16 v[122:125], v[180:183], v[152:155], v[122:125]
	v_mfma_f32_16x16x32_f16 v[114:117], v[184:187], v[152:155], v[114:117]
	global_load_lds_dwordx4 v[196:197], off
	v_lshl_add_u64 v[196:197], v[196:197], 0, s[22:23]
	s_add_u32 m0, s20, 0x6000
	v_mfma_f32_16x16x32_f16 v[110:113], v[188:191], v[152:155], v[110:113]
	v_mfma_f32_16x16x32_f16 v[102:105], v[168:171], v[156:159], v[102:105]
	global_load_lds_dwordx4 v[198:199], off
	v_lshl_add_u64 v[198:199], v[198:199], 0, s[22:23]
	s_add_u32 m0, s20, 0x8000
	v_mfma_f32_16x16x32_f16 v[94:97], v[172:175], v[156:159], v[94:97]
	v_mfma_f32_16x16x32_f16 v[78:81], v[176:179], v[156:159], v[78:81]
	global_load_lds_dwordx4 v[200:201], off
	v_lshl_add_u64 v[200:201], v[200:201], 0, s[22:23]
	s_add_u32 m0, s20, 0xa000
	v_mfma_f32_16x16x32_f16 v[70:73], v[180:183], v[156:159], v[70:73]
	v_mfma_f32_16x16x32_f16 v[62:65], v[184:187], v[156:159], v[62:65]
	global_load_lds_dwordx4 v[202:203], off
	v_lshl_add_u64 v[202:203], v[202:203], 0, s[22:23]
	s_add_u32 m0, s20, 0xc000
	v_mfma_f32_16x16x32_f16 v[58:61], v[188:191], v[156:159], v[58:61]
	v_mfma_f32_16x16x32_f16 v[54:57], v[168:171], v[160:163], v[54:57]
	global_load_lds_dwordx4 v[204:205], off
	v_lshl_add_u64 v[204:205], v[204:205], 0, s[22:23]
	v_add_u32_e32 v206, s15, v150
	v_add_u32_e32 v207, s15, v151
	v_mfma_f32_16x16x32_f16 v[46:49], v[172:175], v[160:163], v[46:49]
	v_mfma_f32_16x16x32_f16 v[42:45], v[176:179], v[160:163], v[42:45]
	ds_read_b128 v[118:121], v206
	v_mfma_f32_16x16x32_f16 v[38:41], v[180:183], v[160:163], v[38:41]
	ds_read_b128 v[98:101], v207 offset:32768
	v_mfma_f32_16x16x32_f16 v[30:33], v[184:187], v[160:163], v[30:33]
	ds_read_b128 v[90:93], v207 offset:34816
	v_mfma_f32_16x16x32_f16 v[26:29], v[188:191], v[160:163], v[26:29]
	ds_read_b128 v[106:109], v206 offset:2048
	v_mfma_f32_16x16x32_f16 v[22:25], v[168:171], v[164:167], v[22:25]
	ds_read_b128 v[82:85], v207 offset:36864
	v_mfma_f32_16x16x32_f16 v[18:21], v[172:175], v[164:167], v[18:21]
	ds_read_b128 v[74:77], v207 offset:38912
	v_mfma_f32_16x16x32_f16 v[14:17], v[176:179], v[164:167], v[14:17]
	ds_read_b128 v[86:89], v206 offset:4096
	v_mfma_f32_16x16x32_f16 v[10:13], v[180:183], v[164:167], v[10:13]
	ds_read_b128 v[66:69], v207 offset:40960
	v_mfma_f32_16x16x32_f16 v[6:9], v[184:187], v[164:167], v[6:9]
	ds_read_b128 v[50:53], v207 offset:43008
	v_mfma_f32_16x16x32_f16 v[2:5], v[188:191], v[164:167], v[2:5]
	ds_read_b128 v[34:37], v206 offset:6144
	s_add_u32 s0, s0, 0x80
	s_addc_u32 s1, s1, 0
	s_cmpk_eq_i32 s0, 0x700
	s_cbranch_scc0 .LBB2_3
	s_add_i32 s0, s15, 0
	v_add3_u32 v0, s0, v147, v148
	s_waitcnt lgkmcnt(0)
	v_mfma_f32_16x16x32_f16 v[134:137], v[98:101], v[118:121], v[134:137]
	s_add_i32 s1, s14, 1
	s_cmp_lg_u32 s1, 2
	s_cselect_b32 s1, s1, 0
	v_mfma_f32_16x16x32_f16 v[130:133], v[90:93], v[118:121], v[130:133]
	v_mfma_f32_16x16x32_f16 v[126:129], v[82:85], v[118:121], v[126:129]
	v_mfma_f32_16x16x32_f16 v[102:105], v[98:101], v[106:109], v[102:105]
	v_mfma_f32_16x16x32_f16 v[94:97], v[90:93], v[106:109], v[94:97]
	v_mfma_f32_16x16x32_f16 v[78:81], v[82:85], v[106:109], v[78:81]
	v_mfma_f32_16x16x32_f16 v[54:57], v[98:101], v[86:89], v[54:57]
	v_mfma_f32_16x16x32_f16 v[46:49], v[90:93], v[86:89], v[46:49]
	v_mfma_f32_16x16x32_f16 v[42:45], v[82:85], v[86:89], v[42:45]
	v_mfma_f32_16x16x32_f16 v[38:41], v[74:77], v[86:89], v[38:41]
	v_mfma_f32_16x16x32_f16 v[30:33], v[66:69], v[86:89], v[30:33]
	v_mfma_f32_16x16x32_f16 v[26:29], v[50:53], v[86:89], v[26:29]
	v_mfma_f32_16x16x32_f16 v[22:25], v[98:101], v[34:37], v[22:25]
	v_mfma_f32_16x16x32_f16 v[18:21], v[90:93], v[34:37], v[18:21]
	ds_read_b128 v[86:89], v0
	ds_read_b128 v[90:93], v0 offset:2048
	v_mfma_f32_16x16x32_f16 v[14:17], v[82:85], v[34:37], v[14:17]
	ds_read_b128 v[82:85], v0 offset:4096
	ds_read_b128 v[98:101], v0 offset:6144
	v_add3_u32 v0, s0, v146, v148
	v_mfma_f32_16x16x32_f16 v[122:125], v[74:77], v[118:121], v[122:125]
	v_mfma_f32_16x16x32_f16 v[114:117], v[66:69], v[118:121], v[114:117]
	v_mfma_f32_16x16x32_f16 v[110:113], v[50:53], v[118:121], v[110:113]
	v_mfma_f32_16x16x32_f16 v[70:73], v[74:77], v[106:109], v[70:73]
	v_mfma_f32_16x16x32_f16 v[62:65], v[66:69], v[106:109], v[62:65]
	v_mfma_f32_16x16x32_f16 v[58:61], v[50:53], v[106:109], v[58:61]
	v_mfma_f32_16x16x32_f16 v[10:13], v[74:77], v[34:37], v[10:13]
	ds_read_b128 v[74:77], v0 offset:32768
	ds_read_b128 v[106:109], v0 offset:34816
	v_mfma_f32_16x16x32_f16 v[6:9], v[66:69], v[34:37], v[6:9]
	ds_read_b128 v[66:69], v0 offset:36864
	ds_read_b128 v[118:121], v0 offset:38912
	ds_read_b128 v[152:155], v0 offset:40960
	ds_read_b128 v[156:159], v0 offset:43008
	v_mfma_f32_16x16x32_f16 v[0:3], v[50:53], v[34:37], v[2:5]
	s_mul_i32 s1, s1, 0xe000
	s_waitcnt vmcnt(0) lgkmcnt(0)
	s_barrier
	v_add_u32_e32 v4, s1, v150
	ds_read_b128 v[34:37], v4
	ds_read_b128 v[50:53], v4 offset:2048
	ds_read_b128 v[160:163], v4 offset:4096
	ds_read_b128 v[164:167], v4 offset:6144
	v_add_u32_e32 v4, s1, v151
	ds_read_b128 v[168:171], v4 offset:32768
	ds_read_b128 v[172:175], v4 offset:34816
	ds_read_b128 v[176:179], v4 offset:36864
	ds_read_b128 v[180:183], v4 offset:38912
	ds_read_b128 v[184:187], v4 offset:40960
	ds_read_b128 v[188:191], v4 offset:43008
	v_mfma_f32_16x16x32_f16 v[134:137], v[74:77], v[86:89], v[134:137]
	v_mfma_f32_16x16x32_f16 v[130:133], v[106:109], v[86:89], v[130:133]
	v_mfma_f32_16x16x32_f16 v[126:129], v[66:69], v[86:89], v[126:129]
	v_mfma_f32_16x16x32_f16 v[122:125], v[118:121], v[86:89], v[122:125]
	v_mfma_f32_16x16x32_f16 v[114:117], v[152:155], v[86:89], v[114:117]
	v_mfma_f32_16x16x32_f16 v[86:89], v[156:159], v[86:89], v[110:113]
	v_mfma_f32_16x16x32_f16 v[102:105], v[74:77], v[90:93], v[102:105]
	v_mfma_f32_16x16x32_f16 v[94:97], v[106:109], v[90:93], v[94:97]
	v_mfma_f32_16x16x32_f16 v[78:81], v[66:69], v[90:93], v[78:81]
	v_mfma_f32_16x16x32_f16 v[70:73], v[118:121], v[90:93], v[70:73]
	v_mfma_f32_16x16x32_f16 v[62:65], v[152:155], v[90:93], v[62:65]
	v_mfma_f32_16x16x32_f16 v[58:61], v[156:159], v[90:93], v[58:61]
	v_mfma_f32_16x16x32_f16 v[54:57], v[74:77], v[82:85], v[54:57]
	v_mfma_f32_16x16x32_f16 v[46:49], v[106:109], v[82:85], v[46:49]
	v_mfma_f32_16x16x32_f16 v[42:45], v[66:69], v[82:85], v[42:45]
	v_mfma_f32_16x16x32_f16 v[38:41], v[118:121], v[82:85], v[38:41]
	v_mfma_f32_16x16x32_f16 v[30:33], v[152:155], v[82:85], v[30:33]
	v_mfma_f32_16x16x32_f16 v[26:29], v[156:159], v[82:85], v[26:29]
	v_mfma_f32_16x16x32_f16 v[22:25], v[74:77], v[98:101], v[22:25]
	v_mfma_f32_16x16x32_f16 v[18:21], v[106:109], v[98:101], v[18:21]
	v_mfma_f32_16x16x32_f16 v[14:17], v[66:69], v[98:101], v[14:17]
	v_mfma_f32_16x16x32_f16 v[10:13], v[118:121], v[98:101], v[10:13]
	v_mfma_f32_16x16x32_f16 v[4:7], v[152:155], v[98:101], v[6:9]
	v_mfma_f32_16x16x32_f16 v[0:3], v[156:159], v[98:101], v[0:3]
	s_add_i32 s0, s1, 0
	s_nop 0
	v_add3_u32 v8, s0, v147, v148
	s_waitcnt lgkmcnt(5)
	v_mfma_f32_16x16x32_f16 v[66:69], v[168:171], v[34:37], v[134:137]
	s_waitcnt lgkmcnt(4)
	v_mfma_f32_16x16x32_f16 v[74:77], v[172:175], v[34:37], v[130:133]
	s_waitcnt lgkmcnt(3)
	v_mfma_f32_16x16x32_f16 v[82:85], v[176:179], v[34:37], v[126:129]
	s_waitcnt lgkmcnt(2)
	v_mfma_f32_16x16x32_f16 v[90:93], v[180:183], v[34:37], v[122:125]
	s_waitcnt lgkmcnt(1)
	v_mfma_f32_16x16x32_f16 v[98:101], v[184:187], v[34:37], v[114:117]
	s_waitcnt lgkmcnt(0)
	v_mfma_f32_16x16x32_f16 v[34:37], v[188:191], v[34:37], v[86:89]
	v_mfma_f32_16x16x32_f16 v[86:89], v[168:171], v[50:53], v[102:105]
	v_mfma_f32_16x16x32_f16 v[94:97], v[172:175], v[50:53], v[94:97]
	v_mfma_f32_16x16x32_f16 v[78:81], v[176:179], v[50:53], v[78:81]
	v_mfma_f32_16x16x32_f16 v[70:73], v[180:183], v[50:53], v[70:73]
	v_mfma_f32_16x16x32_f16 v[62:65], v[184:187], v[50:53], v[62:65]
	v_mfma_f32_16x16x32_f16 v[50:53], v[188:191], v[50:53], v[58:61]
	s_nop 2
	ds_read_b128 v[58:61], v8
	ds_read_b128 v[102:105], v8 offset:2048
	ds_read_b128 v[106:109], v8 offset:4096
	ds_read_b128 v[110:113], v8 offset:6144
	v_mfma_f32_16x16x32_f16 v[8:11], v[180:183], v[164:167], v[10:13]
	s_nop 2
	v_add3_u32 v12, s0, v146, v148
	ds_read_b128 v[114:117], v12 offset:32768
	ds_read_b128 v[118:121], v12 offset:34816
	ds_read_b128 v[122:125], v12 offset:36864
	ds_read_b128 v[126:129], v12 offset:38912
	ds_read_b128 v[130:133], v12 offset:40960
	ds_read_b128 v[134:137], v12 offset:43008
	v_mfma_f32_16x16x32_f16 v[54:57], v[168:171], v[160:163], v[54:57]
	v_mfma_f32_16x16x32_f16 v[46:49], v[172:175], v[160:163], v[46:49]
	v_mfma_f32_16x16x32_f16 v[42:45], v[176:179], v[160:163], v[42:45]
	v_mfma_f32_16x16x32_f16 v[38:41], v[180:183], v[160:163], v[38:41]
	v_mfma_f32_16x16x32_f16 v[30:33], v[184:187], v[160:163], v[30:33]
	v_mfma_f32_16x16x32_f16 v[26:29], v[188:191], v[160:163], v[26:29]
	v_mfma_f32_16x16x32_f16 v[22:25], v[168:171], v[164:167], v[22:25]
	v_mfma_f32_16x16x32_f16 v[18:21], v[172:175], v[164:167], v[18:21]
	v_mfma_f32_16x16x32_f16 v[14:17], v[176:179], v[164:167], v[14:17]
	v_mfma_f32_16x16x32_f16 v[4:7], v[184:187], v[164:167], v[4:7]
	v_mfma_f32_16x16x32_f16 v[0:3], v[188:191], v[164:167], v[0:3]
	s_waitcnt vmcnt(0) lgkmcnt(0)
	s_barrier
	v_mfma_f32_16x16x32_f16 v[66:69], v[114:117], v[58:61], v[66:69]
	v_mfma_f32_16x16x32_f16 v[74:77], v[118:121], v[58:61], v[74:77]
	v_mfma_f32_16x16x32_f16 v[82:85], v[122:125], v[58:61], v[82:85]
	v_mfma_f32_16x16x32_f16 v[90:93], v[126:129], v[58:61], v[90:93]
	v_mfma_f32_16x16x32_f16 v[98:101], v[130:133], v[58:61], v[98:101]
	v_mfma_f32_16x16x32_f16 v[34:37], v[134:137], v[58:61], v[34:37]
	v_mfma_f32_16x16x32_f16 v[58:61], v[114:117], v[102:105], v[86:89]
	v_mfma_f32_16x16x32_f16 v[86:89], v[118:121], v[102:105], v[94:97]
	v_mfma_f32_16x16x32_f16 v[78:81], v[122:125], v[102:105], v[78:81]
	v_mfma_f32_16x16x32_f16 v[70:73], v[126:129], v[102:105], v[70:73]
	v_mfma_f32_16x16x32_f16 v[62:65], v[130:133], v[102:105], v[62:65]
	v_mfma_f32_16x16x32_f16 v[50:53], v[134:137], v[102:105], v[50:53]
	v_mfma_f32_16x16x32_f16 v[54:57], v[114:117], v[106:109], v[54:57]
	v_mfma_f32_16x16x32_f16 v[46:49], v[118:121], v[106:109], v[46:49]
	v_mfma_f32_16x16x32_f16 v[42:45], v[122:125], v[106:109], v[42:45]
	v_mfma_f32_16x16x32_f16 v[38:41], v[126:129], v[106:109], v[38:41]
	v_mfma_f32_16x16x32_f16 v[30:33], v[130:133], v[106:109], v[30:33]
	v_mfma_f32_16x16x32_f16 v[26:29], v[134:137], v[106:109], v[26:29]
	v_mfma_f32_16x16x32_f16 v[22:25], v[114:117], v[110:113], v[22:25]
	v_mfma_f32_16x16x32_f16 v[18:21], v[118:121], v[110:113], v[18:21]
	v_mfma_f32_16x16x32_f16 v[12:15], v[122:125], v[110:113], v[14:17]
	v_mfma_f32_16x16x32_f16 v[8:11], v[126:129], v[110:113], v[8:11]
	v_mfma_f32_16x16x32_f16 v[4:7], v[130:133], v[110:113], v[4:7]
	v_mfma_f32_16x16x32_f16 v[0:3], v[134:137], v[110:113], v[0:3]
	s_movk_i32 s0, 0x3400
	v_mad_u32_u24 v94, v144, s0, 0
	v_lshlrev_b32_e32 v16, 3, v145
	v_mul_u32_u24_e32 v17, 0xd0, v143
	v_add3_u32 v95, v94, v16, v17
	v_cvt_pk_f16_f32 v17, v68, v69
	v_cvt_pk_f16_f32 v16, v66, v67
	v_cvt_pk_f16_f32 v67, v76, v77
	v_cvt_pk_f16_f32 v66, v74, v75
	s_barrier
	ds_write2_b64 v95, v[16:17], v[66:67] offset1:4
	v_cvt_pk_f16_f32 v17, v84, v85
	v_cvt_pk_f16_f32 v16, v82, v83
	v_cvt_pk_f16_f32 v67, v92, v93
	v_cvt_pk_f16_f32 v66, v90, v91
	s_mov_b32 s0, 0x15555556
	ds_write2_b64 v95, v[16:17], v[66:67] offset0:8 offset1:12
	v_cvt_pk_f16_f32 v17, v100, v101
	v_cvt_pk_f16_f32 v16, v98, v99
	v_cvt_pk_f16_f32 v37, v36, v37
	v_cvt_pk_f16_f32 v36, v34, v35
	v_cvt_pk_f16_f32 v7, v6, v7
	v_cvt_pk_f16_f32 v6, v4, v5
	v_mul_hi_u32 v4, v140, s0
	ds_write2_b64 v95, v[16:17], v[36:37] offset0:16 offset1:20
	v_cvt_pk_f16_f32 v17, v60, v61
	v_cvt_pk_f16_f32 v16, v58, v59
	v_cvt_pk_f16_f32 v35, v88, v89
	v_cvt_pk_f16_f32 v34, v86, v87
	v_add_u32_e32 v36, 0x800, v95
	v_cvt_pk_f16_f32 v21, v20, v21
	v_cvt_pk_f16_f32 v20, v18, v19
	v_add_u32_e32 v18, 0x2000, v95
	v_cvt_pk_f16_f32 v15, v14, v15
	v_cvt_pk_f16_f32 v14, v12, v13
	v_cvt_pk_f16_f32 v11, v10, v11
	v_cvt_pk_f16_f32 v10, v8, v9
	v_cvt_pk_f16_f32 v3, v2, v3
	v_cvt_pk_f16_f32 v2, v0, v1
	v_mul_u32_u24_e32 v0, 12, v4
	ds_write2_b64 v36, v[16:17], v[34:35] offset0:160 offset1:164
	v_cvt_pk_f16_f32 v17, v80, v81
	v_cvt_pk_f16_f32 v16, v78, v79
	v_cvt_pk_f16_f32 v35, v72, v73
	v_cvt_pk_f16_f32 v34, v70, v71
	ds_write2_b64 v18, v[14:15], v[10:11] offset0:232 offset1:236
	v_add_u32_e32 v10, s13, v142
	v_sub_u32_e32 v5, v140, v0
	ds_write2_b64 v36, v[16:17], v[34:35] offset0:168 offset1:172
	v_cvt_pk_f16_f32 v17, v64, v65
	v_cvt_pk_f16_f32 v16, v62, v63
	v_cvt_pk_f16_f32 v35, v52, v53
	v_cvt_pk_f16_f32 v34, v50, v51
	v_lshl_add_u32 v12, v5, 3, v10
	ds_write2_b64 v36, v[16:17], v[34:35] offset0:176 offset1:180
	v_cvt_pk_f16_f32 v17, v56, v57
	v_cvt_pk_f16_f32 v16, v54, v55
	v_cvt_pk_f16_f32 v35, v48, v49
	v_cvt_pk_f16_f32 v34, v46, v47
	v_add_u32_e32 v36, 0x1800, v95
	v_lshrrev_b32_e32 v0, 10, v12
	v_mov_b32_e32 v1, 0
	ds_write2_b64 v36, v[16:17], v[34:35] offset0:64 offset1:68
	v_cvt_pk_f16_f32 v17, v44, v45
	v_cvt_pk_f16_f32 v16, v42, v43
	v_cvt_pk_f16_f32 v35, v40, v41
	v_cvt_pk_f16_f32 v34, v38, v39
	ds_write2_b64 v18, v[6:7], v[2:3] offset0:240 offset1:244
	v_add_u32_e32 v11, s12, v141
	v_lshlrev_b64 v[2:3], 23, v[0:1]
	ds_write2_b64 v36, v[16:17], v[34:35] offset0:72 offset1:76
	v_cvt_pk_f16_f32 v17, v32, v33
	v_cvt_pk_f16_f32 v16, v30, v31
	v_cvt_pk_f16_f32 v29, v28, v29
	v_cvt_pk_f16_f32 v28, v26, v27
	v_lshl_add_u64 v[6:7], s[8:9], 0, v[2:3]
	v_or_b32_e32 v2, v11, v4
	ds_write2_b64 v36, v[16:17], v[28:29] offset0:80 offset1:84
	v_cvt_pk_f16_f32 v17, v24, v25
	v_cvt_pk_f16_f32 v16, v22, v23
	v_ashrrev_i32_e32 v3, 31, v2
	ds_write2_b64 v18, v[16:17], v[20:21] offset0:224 offset1:228
	v_lshlrev_b64 v[8:9], 11, v[2:3]
	v_mul_u32_u24_e32 v0, 0xd0, v4
	v_lshlrev_b32_e32 v2, 4, v5
	s_waitcnt lgkmcnt(0)
	v_add3_u32 v0, v94, v0, v2
	ds_read_b128 v[2:5], v0
	v_and_b32_e32 v0, 0x3f8, v12
	v_lshl_add_u64 v[6:7], v[6:7], 0, v[8:9]
	v_lshlrev_b32_e32 v0, 1, v0
	v_lshl_add_u64 v[6:7], v[6:7], 0, v[0:1]
	v_or_b32_e32 v0, 64, v140
	s_waitcnt lgkmcnt(0)
	global_store_dwordx4 v[6:7], v[2:5], off sc1
	s_nop 1
	v_mul_hi_u32 v4, v0, s0
	v_mul_u32_u24_e32 v2, 12, v4
	v_sub_u32_e32 v5, v0, v2
	v_lshl_add_u32 v12, v5, 3, v10
	v_lshrrev_b32_e32 v0, 10, v12
	v_lshlrev_b64 v[2:3], 23, v[0:1]
	v_lshl_add_u64 v[6:7], s[8:9], 0, v[2:3]
	v_or_b32_e32 v2, v11, v4
	v_ashrrev_i32_e32 v3, 31, v2
	v_lshlrev_b64 v[8:9], 11, v[2:3]
	v_mul_u32_u24_e32 v0, 0xd0, v4
	v_lshlrev_b32_e32 v2, 4, v5
	v_add3_u32 v0, v94, v0, v2
	ds_read_b128 v[2:5], v0
	v_and_b32_e32 v0, 0x3f8, v12
	v_lshl_add_u64 v[6:7], v[6:7], 0, v[8:9]
	v_lshlrev_b32_e32 v0, 1, v0
	v_lshl_add_u64 v[6:7], v[6:7], 0, v[0:1]
	v_or_b32_e32 v0, 0x80, v140
	s_waitcnt lgkmcnt(0)
	global_store_dwordx4 v[6:7], v[2:5], off sc1
	s_nop 1
	v_mul_hi_u32 v4, v0, s0
	v_mul_u32_u24_e32 v2, 12, v4
	v_sub_u32_e32 v5, v0, v2
	v_lshl_add_u32 v12, v5, 3, v10
	v_lshrrev_b32_e32 v0, 10, v12
	v_lshlrev_b64 v[2:3], 23, v[0:1]
	v_lshl_add_u64 v[6:7], s[8:9], 0, v[2:3]
	v_or_b32_e32 v2, v11, v4
	v_ashrrev_i32_e32 v3, 31, v2
	v_lshlrev_b64 v[8:9], 11, v[2:3]
	v_mul_u32_u24_e32 v0, 0xd0, v4
	v_lshlrev_b32_e32 v2, 4, v5
	v_add3_u32 v0, v94, v0, v2
	ds_read_b128 v[2:5], v0
	v_and_b32_e32 v0, 0x3f8, v12
	v_lshl_add_u64 v[6:7], v[6:7], 0, v[8:9]
	v_lshlrev_b32_e32 v0, 1, v0
	v_lshl_add_u64 v[6:7], v[6:7], 0, v[0:1]
	v_or_b32_e32 v0, 0xc0, v140
	s_waitcnt lgkmcnt(0)
	global_store_dwordx4 v[6:7], v[2:5], off sc1
	s_nop 1
	v_mul_hi_u32 v4, v0, s0
	v_mul_u32_u24_e32 v2, 12, v4
	v_sub_u32_e32 v5, v0, v2
	v_lshl_add_u32 v12, v5, 3, v10
	v_lshrrev_b32_e32 v0, 10, v12
	v_lshlrev_b64 v[2:3], 23, v[0:1]
	v_lshl_add_u64 v[6:7], s[8:9], 0, v[2:3]
	v_or_b32_e32 v2, v11, v4
	v_ashrrev_i32_e32 v3, 31, v2
	v_lshlrev_b64 v[8:9], 11, v[2:3]
	v_mul_u32_u24_e32 v0, 0xd0, v4
	v_lshlrev_b32_e32 v2, 4, v5
	v_add3_u32 v0, v94, v0, v2
	ds_read_b128 v[2:5], v0
	v_and_b32_e32 v0, 0x3f8, v12
	v_lshl_add_u64 v[6:7], v[6:7], 0, v[8:9]
	v_lshlrev_b32_e32 v0, 1, v0
	v_lshl_add_u64 v[6:7], v[6:7], 0, v[0:1]
	v_or_b32_e32 v0, 0x100, v140
	s_waitcnt lgkmcnt(0)
	global_store_dwordx4 v[6:7], v[2:5], off sc1
	s_nop 1
	v_mul_hi_u32 v4, v0, s0
	v_mul_u32_u24_e32 v2, 12, v4
	v_sub_u32_e32 v5, v0, v2
	v_lshl_add_u32 v12, v5, 3, v10
	v_lshrrev_b32_e32 v0, 10, v12
	v_lshlrev_b64 v[2:3], 23, v[0:1]
	v_lshl_add_u64 v[6:7], s[8:9], 0, v[2:3]
	v_or_b32_e32 v2, v11, v4
	v_ashrrev_i32_e32 v3, 31, v2
	v_lshlrev_b64 v[8:9], 11, v[2:3]
	v_mul_u32_u24_e32 v0, 0xd0, v4
	v_lshlrev_b32_e32 v2, 4, v5
	v_add3_u32 v0, v94, v0, v2
	ds_read_b128 v[2:5], v0
	v_and_b32_e32 v0, 0x3f8, v12
	v_lshl_add_u64 v[6:7], v[6:7], 0, v[8:9]
	v_lshlrev_b32_e32 v0, 1, v0
	v_lshl_add_u64 v[6:7], v[6:7], 0, v[0:1]
	v_or_b32_e32 v0, 0x140, v140
	s_waitcnt lgkmcnt(0)
	global_store_dwordx4 v[6:7], v[2:5], off sc1
	s_nop 1
	v_mul_hi_u32 v4, v0, s0
	v_mul_u32_u24_e32 v2, 12, v4
	v_sub_u32_e32 v5, v0, v2
	v_lshl_add_u32 v12, v5, 3, v10
	v_lshrrev_b32_e32 v0, 10, v12
	v_lshlrev_b64 v[2:3], 23, v[0:1]
	v_lshl_add_u64 v[6:7], s[8:9], 0, v[2:3]
	v_or_b32_e32 v2, v11, v4
	v_ashrrev_i32_e32 v3, 31, v2
	v_lshlrev_b64 v[8:9], 11, v[2:3]
	v_mul_u32_u24_e32 v0, 0xd0, v4
	v_lshlrev_b32_e32 v2, 4, v5
	v_add3_u32 v0, v94, v0, v2
	ds_read_b128 v[2:5], v0
	v_and_b32_e32 v0, 0x3f8, v12
	v_lshl_add_u64 v[6:7], v[6:7], 0, v[8:9]
	v_lshlrev_b32_e32 v0, 1, v0
	v_lshl_add_u64 v[6:7], v[6:7], 0, v[0:1]
	v_or_b32_e32 v0, 0x180, v140
	s_waitcnt lgkmcnt(0)
	global_store_dwordx4 v[6:7], v[2:5], off sc1
	s_nop 1
	v_mul_hi_u32 v4, v0, s0
	v_mul_u32_u24_e32 v2, 12, v4
	v_sub_u32_e32 v5, v0, v2
	v_lshl_add_u32 v12, v5, 3, v10
	v_lshrrev_b32_e32 v0, 10, v12
	v_lshlrev_b64 v[2:3], 23, v[0:1]
	v_lshl_add_u64 v[6:7], s[8:9], 0, v[2:3]
	v_or_b32_e32 v2, v11, v4
	v_ashrrev_i32_e32 v3, 31, v2
	v_lshlrev_b64 v[8:9], 11, v[2:3]
	v_mul_u32_u24_e32 v0, 0xd0, v4
	v_lshlrev_b32_e32 v2, 4, v5
	v_add3_u32 v0, v94, v0, v2
	ds_read_b128 v[2:5], v0
	v_and_b32_e32 v0, 0x3f8, v12
	v_lshl_add_u64 v[6:7], v[6:7], 0, v[8:9]
	v_lshlrev_b32_e32 v0, 1, v0
	v_lshl_add_u64 v[6:7], v[6:7], 0, v[0:1]
	v_or_b32_e32 v0, 0x1c0, v140
	s_waitcnt lgkmcnt(0)
	global_store_dwordx4 v[6:7], v[2:5], off sc1
	s_nop 1
	v_mul_hi_u32 v4, v0, s0
	v_mul_u32_u24_e32 v2, 12, v4
	v_sub_u32_e32 v5, v0, v2
	v_lshl_add_u32 v12, v5, 3, v10
	v_lshrrev_b32_e32 v0, 10, v12
	v_lshlrev_b64 v[2:3], 23, v[0:1]
	v_lshl_add_u64 v[6:7], s[8:9], 0, v[2:3]
	v_or_b32_e32 v2, v11, v4
	v_ashrrev_i32_e32 v3, 31, v2
	v_lshlrev_b64 v[8:9], 11, v[2:3]
	v_mul_u32_u24_e32 v0, 0xd0, v4
	v_lshlrev_b32_e32 v2, 4, v5
	v_add3_u32 v0, v94, v0, v2
	ds_read_b128 v[2:5], v0
	v_and_b32_e32 v0, 0x3f8, v12
	v_lshl_add_u64 v[6:7], v[6:7], 0, v[8:9]
	v_lshlrev_b32_e32 v0, 1, v0
	v_lshl_add_u64 v[6:7], v[6:7], 0, v[0:1]
	v_or_b32_e32 v0, 0x200, v140
	s_waitcnt lgkmcnt(0)
	global_store_dwordx4 v[6:7], v[2:5], off sc1
	s_nop 1
	v_mul_hi_u32 v4, v0, s0
	v_mul_u32_u24_e32 v2, 12, v4
	v_sub_u32_e32 v5, v0, v2
	v_lshl_add_u32 v12, v5, 3, v10
	v_lshrrev_b32_e32 v0, 10, v12
	v_lshlrev_b64 v[2:3], 23, v[0:1]
	v_lshl_add_u64 v[6:7], s[8:9], 0, v[2:3]
	v_or_b32_e32 v2, v11, v4
	v_ashrrev_i32_e32 v3, 31, v2
	v_lshlrev_b64 v[8:9], 11, v[2:3]
	v_mul_u32_u24_e32 v0, 0xd0, v4
	v_lshlrev_b32_e32 v2, 4, v5
	v_add3_u32 v0, v94, v0, v2
	ds_read_b128 v[2:5], v0
	v_and_b32_e32 v0, 0x3f8, v12
	v_lshl_add_u64 v[6:7], v[6:7], 0, v[8:9]
	v_lshlrev_b32_e32 v0, 1, v0
	v_lshl_add_u64 v[6:7], v[6:7], 0, v[0:1]
	v_or_b32_e32 v0, 0x240, v140
	s_waitcnt lgkmcnt(0)
	global_store_dwordx4 v[6:7], v[2:5], off sc1
	s_nop 1
	v_mul_hi_u32 v4, v0, s0
	v_mul_u32_u24_e32 v2, 12, v4
	v_sub_u32_e32 v5, v0, v2
	v_lshl_add_u32 v12, v5, 3, v10
	v_lshrrev_b32_e32 v0, 10, v12
	v_lshlrev_b64 v[2:3], 23, v[0:1]
	v_lshl_add_u64 v[6:7], s[8:9], 0, v[2:3]
	v_or_b32_e32 v2, v11, v4
	v_ashrrev_i32_e32 v3, 31, v2
	v_lshlrev_b64 v[8:9], 11, v[2:3]
	v_mul_u32_u24_e32 v0, 0xd0, v4
	v_lshlrev_b32_e32 v2, 4, v5
	v_add3_u32 v0, v94, v0, v2
	ds_read_b128 v[2:5], v0
	v_and_b32_e32 v0, 0x3f8, v12
	v_lshl_add_u64 v[6:7], v[6:7], 0, v[8:9]
	v_lshlrev_b32_e32 v0, 1, v0
	v_lshl_add_u64 v[6:7], v[6:7], 0, v[0:1]
	v_or_b32_e32 v0, 0x280, v140
	s_waitcnt lgkmcnt(0)
	global_store_dwordx4 v[6:7], v[2:5], off sc1
	s_nop 1
	v_mul_hi_u32 v4, v0, s0
	v_mul_u32_u24_e32 v2, 12, v4
	v_sub_u32_e32 v5, v0, v2
	v_lshl_add_u32 v12, v5, 3, v10
	v_lshrrev_b32_e32 v0, 10, v12
	v_lshlrev_b64 v[2:3], 23, v[0:1]
	v_lshl_add_u64 v[6:7], s[8:9], 0, v[2:3]
	v_or_b32_e32 v2, v11, v4
	v_ashrrev_i32_e32 v3, 31, v2
	v_lshlrev_b64 v[8:9], 11, v[2:3]
	v_mul_u32_u24_e32 v0, 0xd0, v4
	v_lshlrev_b32_e32 v2, 4, v5
	v_add3_u32 v0, v94, v0, v2
	ds_read_b128 v[2:5], v0
	v_and_b32_e32 v0, 0x3f8, v12
	v_lshl_add_u64 v[6:7], v[6:7], 0, v[8:9]
	v_lshlrev_b32_e32 v0, 1, v0
	v_lshl_add_u64 v[6:7], v[6:7], 0, v[0:1]
	v_or_b32_e32 v0, 0x2c0, v140
	s_waitcnt lgkmcnt(0)
	global_store_dwordx4 v[6:7], v[2:5], off sc1
	s_nop 1
	v_mul_hi_u32 v4, v0, s0
	v_mul_u32_u24_e32 v2, 12, v4
	v_sub_u32_e32 v5, v0, v2
	v_lshl_add_u32 v10, v5, 3, v10
	v_lshrrev_b32_e32 v0, 10, v10
	v_lshlrev_b64 v[2:3], 23, v[0:1]
	v_lshl_add_u64 v[6:7], s[8:9], 0, v[2:3]
	v_or_b32_e32 v2, v11, v4
	v_ashrrev_i32_e32 v3, 31, v2
	v_lshlrev_b64 v[8:9], 11, v[2:3]
	v_mul_u32_u24_e32 v0, 0xd0, v4
	v_lshlrev_b32_e32 v2, 4, v5
	v_add3_u32 v0, v94, v0, v2
	ds_read_b128 v[2:5], v0
	v_and_b32_e32 v0, 0x3f8, v10
	v_lshl_add_u64 v[6:7], v[6:7], 0, v[8:9]
	v_lshlrev_b32_e32 v0, 1, v0
	v_lshl_add_u64 v[0:1], v[6:7], 0, v[0:1]
	s_waitcnt lgkmcnt(0)
	global_store_dwordx4 v[0:1], v[2:5], off sc1
	s_nop 1
	s_endpgm
	s_nop 0
	s_nop 0
	s_nop 0
	s_nop 0
	s_nop 0
	s_nop 0
	s_nop 0
	s_nop 0
	s_nop 0
	s_nop 0
	s_nop 0
	s_nop 0
	s_nop 0
	s_nop 0
	s_nop 0
	s_nop 0
	s_nop 0
	s_nop 0
	s_nop 0
	s_nop 0
	s_nop 0
	s_nop 0
	s_nop 0
	s_nop 0
	s_nop 0
	s_nop 0
	s_nop 0
	s_nop 0
	s_nop 0
	s_nop 0
	s_nop 0
	s_nop 0
	s_nop 0
	s_nop 0
	s_nop 0
	s_nop 0
	s_nop 0
	s_nop 0
	s_nop 0
	s_nop 0
	s_nop 0
	s_nop 0
	s_nop 0
	s_nop 0
	s_nop 0
	s_nop 0
	s_nop 0
	s_nop 0
	s_endpgm

	.amdhsa_kernel _Z8gemm16_kILi256ELi192ELi0ELi2EEvPKDF16_S1_PvPKfi
		.amdhsa_group_segment_fixed_size 0
		.amdhsa_private_segment_fixed_size 0
		.amdhsa_kernarg_size 36
		.amdhsa_user_sgpr_count 2
		.amdhsa_user_sgpr_dispatch_ptr 0
		.amdhsa_user_sgpr_queue_ptr 0
		.amdhsa_user_sgpr_kernarg_segment_ptr 1
		.amdhsa_user_sgpr_dispatch_id 0
		.amdhsa_user_sgpr_kernarg_preload_length 0
		.amdhsa_user_sgpr_kernarg_preload_offset 0
		.amdhsa_user_sgpr_private_segment_size 0
		.amdhsa_uses_dynamic_stack 0
		.amdhsa_enable_private_segment 0
		.amdhsa_system_sgpr_workgroup_id_x 1
		.amdhsa_system_sgpr_workgroup_id_y 0
		.amdhsa_system_sgpr_workgroup_id_z 0
		.amdhsa_system_sgpr_workgroup_info 0
		.amdhsa_system_vgpr_workitem_id 0
		.amdhsa_next_free_vgpr 208
		.amdhsa_next_free_sgpr 24
		.amdhsa_accum_offset 208
		.amdhsa_reserve_vcc 1
		.amdhsa_float_round_mode_32 0
		.amdhsa_float_round_mode_16_64 0
		.amdhsa_float_denorm_mode_32 3
		.amdhsa_float_denorm_mode_16_64 3
		.amdhsa_dx10_clamp 1
		.amdhsa_ieee_mode 1
		.amdhsa_fp16_overflow 0
		.amdhsa_tg_split 0
		.amdhsa_exception_fp_ieee_invalid_op 0
		.amdhsa_exception_fp_denorm_src 0
		.amdhsa_exception_fp_ieee_div_zero 0
		.amdhsa_exception_fp_ieee_overflow 0
		.amdhsa_exception_fp_ieee_underflow 0
		.amdhsa_exception_fp_ieee_inexact 0
		.amdhsa_exception_int_div_zero 0
	.end_amdhsa_kernel

amdhsa.kernels:
  - .agpr_count:     0
    .args:
      - .address_space:  global
        .offset:         0
        .size:           8
        .value_kind:     global_buffer
      - .address_space:  global
        .offset:         8
        .size:           8
        .value_kind:     global_buffer
      - .address_space:  global
        .offset:         16
        .size:           8
        .value_kind:     global_buffer
      - .address_space:  global
        .offset:         24
        .size:           8
        .value_kind:     global_buffer
      - .address_space:  global
        .offset:         32
        .size:           8
        .value_kind:     global_buffer
      - .address_space:  global
        .offset:         40
        .size:           8
        .value_kind:     global_buffer
      - .address_space:  global
        .offset:         48
        .size:           8
        .value_kind:     global_buffer
      - .address_space:  global
        .offset:         56
        .size:           8
        .value_kind:     global_buffer
    .group_segment_fixed_size: 0
    .kernarg_segment_align: 8
    .kernarg_segment_size: 64
    .language:       OpenCL C
    .language_version:
      - 2
      - 0
    .max_flat_workgroup_size: 256
    .name:           _Z10cvt_kernelPKfS0_S0_S0_S0_PDF16_S1_S1_
    .private_segment_fixed_size: 0
    .sgpr_count:     20
    .sgpr_spill_count: 0
    .symbol:         _Z10cvt_kernelPKfS0_S0_S0_S0_PDF16_S1_S1_.kd
    .uniform_work_group_size: 1
    .uses_dynamic_stack: false
    .vgpr_count:     70
    .vgpr_spill_count: 0
    .wavefront_size: 64
  - .agpr_count:     0
    .args:
      - .address_space:  global
        .offset:         0
        .size:           8
        .value_kind:     global_buffer
      - .address_space:  global
        .offset:         8
        .size:           8
        .value_kind:     global_buffer
      - .address_space:  global
        .offset:         16
        .size:           8
        .value_kind:     global_buffer
      - .address_space:  global
        .offset:         24
        .size:           8
        .value_kind:     global_buffer
    .group_segment_fixed_size: 0
    .kernarg_segment_align: 8
    .kernarg_segment_size: 32
    .language:       OpenCL C
    .language_version:
      - 2
      - 0
    .max_flat_workgroup_size: 512
    .name:           _Z10attn64_fwdPKDF16_S0_S0_PDF16_
    .private_segment_fixed_size: 0
    .sgpr_count:     57
    .sgpr_spill_count: 0
    .symbol:         _Z10attn64_fwdPKDF16_S0_S0_PDF16_.kd
    .uniform_work_group_size: 1
    .uses_dynamic_stack: false
    .vgpr_count:     219
    .vgpr_spill_count: 0
    .wavefront_size: 64
  - .agpr_count:     0
    .args:
      - .address_space:  global
        .offset:         0
        .size:           8
        .value_kind:     global_buffer
      - .address_space:  global
        .offset:         8
        .size:           8
        .value_kind:     global_buffer
      - .address_space:  global
        .offset:         16
        .size:           8
        .value_kind:     global_buffer
      - .actual_access:  read_only
        .address_space:  global
        .offset:         24
        .size:           8
        .value_kind:     global_buffer
      - .offset:         32
        .size:           4
        .value_kind:     by_value
    .group_segment_fixed_size: 0
    .kernarg_segment_align: 8
    .kernarg_segment_size: 36
    .language:       OpenCL C
    .language_version:
      - 2
      - 0
    .max_flat_workgroup_size: 512
    .name:           _Z8gemm16_kILi256ELi192ELi0ELi2EEvPKDF16_S1_PvPKfi
    .private_segment_fixed_size: 0
    .sgpr_count:     30
    .sgpr_spill_count: 0
    .symbol:         _Z8gemm16_kILi256ELi192ELi0ELi2EEvPKDF16_S1_PvPKfi.kd
    .uniform_work_group_size: 1
    .uses_dynamic_stack: false
    .vgpr_count:     208
    .vgpr_spill_count: 0
    .wavefront_size: 64
  - .agpr_count:     0
    .args:
      - .address_space:  global
        .offset:         0
        .size:           8
        .value_kind:     global_buffer
      - .address_space:  global
        .offset:         8
        .size:           8
        .value_kind:     global_buffer
      - .address_space:  global
        .offset:         16
        .size:           8
        .value_kind:     global_buffer
      - .actual_access:  read_only
        .address_space:  global
        .offset:         24
        .size:           8
        .value_kind:     global_buffer
      - .offset:         32
        .size:           4
        .value_kind:     by_value
    .group_segment_fixed_size: 0
    .kernarg_segment_align: 8
    .kernarg_segment_size: 36
    .language:       OpenCL C
    .language_version:
      - 2
      - 0
    .max_flat_workgroup_size: 512
    .name:           _Z8gemm16_kILi128ELi128ELi1ELi3EEvPKDF16_S1_PvPKfi
    .private_segment_fixed_size: 0
    .sgpr_count:     28
    .sgpr_spill_count: 0
    .symbol:         _Z8gemm16_kILi128ELi128ELi1ELi3EEvPKDF16_S1_PvPKfi.kd
    .uniform_work_group_size: 1
    .uses_dynamic_stack: false
    .vgpr_count:     104
    .vgpr_spill_count: 0
    .wavefront_size: 64
